# non-temporal hint on the weight-conversion loops' global loads and stores (streaming data, read once / written once)
# baseline (speedup 1.0000x reference)
.LBB0_218:
	v_add_u32_e32 v2, 0x800, v130
	s_lshr_b32 s0, s12, 8
	v_ashrrev_i32_e32 v41, 6, v2
	v_cvt_f32_u32_e32 v2, s0
	s_sub_i32 s13, 0, s0
	s_abs_i32 s9, s14
	s_ashr_i32 s8, s14, 31
	v_rcp_iflag_f32_e32 v2, v2
	v_add_u32_e32 v3, 0xa00, v130
	v_ashrrev_i32_e32 v42, 6, v3
	v_add_u32_e32 v3, 0xc00, v130
	v_mul_f32_e32 v2, 0x4f7ffffe, v2
	v_cvt_u32_f32_e32 v2, v2
	v_lshlrev_b32_e32 v1, 2, v130
	v_ashrrev_i32_e32 v43, 6, v3
	v_add_u32_e32 v3, 0xe00, v130
	v_readfirstlane_b32 s15, v2
	s_mul_i32 s13, s13, s15
	s_mul_hi_u32 s13, s15, s13
	s_add_i32 s15, s15, s13
	s_mul_hi_u32 s13, s9, s15
	s_mul_i32 s15, s13, s0
	s_sub_i32 s9, s9, s15
	s_add_i32 s15, s13, 1
	s_sub_i32 s16, s9, s0
	s_cmp_ge_u32 s9, s0
	s_cselect_b32 s13, s15, s13
	s_cselect_b32 s9, s16, s9
	s_add_i32 s15, s13, 1
	s_cmp_ge_u32 s9, s0
	s_cselect_b32 s9, s15, s13
	s_xor_b32 s9, s9, s8
	s_sub_i32 s13, s9, s8
	s_mul_i32 s0, s13, s0
	s_sub_i32 s0, s14, s0
	s_lshl_b32 s8, s0, 8
	s_ashr_i32 s9, s8, 31
	s_lshl_b64 s[14:15], s[8:9], 2
	s_add_u32 s10, s10, s14
	v_and_b32_e32 v36, 0xfc, v1
	v_ashrrev_i32_e32 v44, 6, v3
	s_addc_u32 s11, s11, s15
	s_lshl_b32 s16, s13, 6
	v_mov_b32_e32 v35, 0
	v_lshlrev_b32_e32 v34, 2, v36
	v_add_u32_e32 v4, s16, v44
	v_lshl_add_u64 v[2:3], s[10:11], 0, v[34:35]
	v_ashrrev_i32_e32 v7, 31, v4
	v_mad_u64_u32 v[4:5], s[10:11], v4, s12, 0
	v_mov_b32_e32 v6, v5
	v_mad_u64_u32 v[6:7], s[10:11], v7, s12, v[6:7]
	v_mov_b32_e32 v5, v6
	v_add_u32_e32 v6, s16, v43
	v_ashrrev_i32_e32 v9, 31, v6
	v_mad_u64_u32 v[6:7], s[10:11], v6, s12, 0
	v_mov_b32_e32 v8, v7
	v_mad_u64_u32 v[8:9], s[10:11], v9, s12, v[8:9]
	v_lshl_add_u64 v[4:5], v[4:5], 2, v[2:3]
	v_mov_b32_e32 v7, v8
	v_lshl_add_u64 v[6:7], v[6:7], 2, v[2:3]
	global_load_dwordx4 v[30:33], v[4:5], off nt
	global_load_dwordx4 v[26:29], v[6:7], off nt
	v_add_u32_e32 v4, s16, v42
	v_ashrrev_i32_e32 v7, 31, v4
	v_mad_u64_u32 v[4:5], s[10:11], v4, s12, 0
	v_mov_b32_e32 v6, v5
	v_mad_u64_u32 v[6:7], s[10:11], v7, s12, v[6:7]
	v_mov_b32_e32 v5, v6
	v_add_u32_e32 v6, s16, v41
	v_ashrrev_i32_e32 v9, 31, v6
	v_mad_u64_u32 v[6:7], s[10:11], v6, s12, 0
	v_mov_b32_e32 v8, v7
	v_add_u32_e32 v54, 0x600, v130
	v_mad_u64_u32 v[8:9], s[10:11], v9, s12, v[8:9]
	v_ashrrev_i32_e32 v40, 6, v54
	v_lshl_add_u64 v[4:5], v[4:5], 2, v[2:3]
	v_mov_b32_e32 v7, v8
	v_lshl_add_u64 v[6:7], v[6:7], 2, v[2:3]
	global_load_dwordx4 v[22:25], v[4:5], off nt
	global_load_dwordx4 v[18:21], v[6:7], off nt
	v_add_u32_e32 v4, s16, v40
	v_ashrrev_i32_e32 v7, 31, v4
	v_mad_u64_u32 v[4:5], s[10:11], v4, s12, 0
	v_add_u32_e32 v51, 0x400, v130
	v_mov_b32_e32 v6, v5
	v_ashrrev_i32_e32 v39, 6, v51
	v_mad_u64_u32 v[6:7], s[10:11], v7, s12, v[6:7]
	v_mov_b32_e32 v5, v6
	v_add_u32_e32 v6, s16, v39
	v_ashrrev_i32_e32 v9, 31, v6
	v_mad_u64_u32 v[6:7], s[10:11], v6, s12, 0
	v_mov_b32_e32 v8, v7
	v_add_u32_e32 v37, 0x200, v130
	v_mad_u64_u32 v[8:9], s[10:11], v9, s12, v[8:9]
	v_ashrrev_i32_e32 v38, 6, v37
	v_lshl_add_u64 v[4:5], v[4:5], 2, v[2:3]
	v_mov_b32_e32 v7, v8
	v_lshl_add_u64 v[6:7], v[6:7], 2, v[2:3]
	global_load_dwordx4 v[14:17], v[4:5], off nt
	global_load_dwordx4 v[10:13], v[6:7], off nt
	v_add_u32_e32 v4, s16, v38
	v_ashrrev_i32_e32 v7, 31, v4
	v_mad_u64_u32 v[4:5], s[10:11], v4, s12, 0
	v_mov_b32_e32 v6, v5
	v_ashrrev_i32_e32 v1, 6, v130
	v_mad_u64_u32 v[6:7], s[10:11], v7, s12, v[6:7]
	v_mov_b32_e32 v5, v6
	v_add_u32_e32 v6, s16, v1
	v_ashrrev_i32_e32 v9, 31, v6
	v_mad_u64_u32 v[6:7], s[10:11], v6, s12, 0
	v_mov_b32_e32 v8, v7
	v_mad_u64_u32 v[8:9], s[10:11], v9, s12, v[8:9]
	v_mov_b32_e32 v7, v8
	v_lshl_add_u64 v[4:5], v[4:5], 2, v[2:3]
	v_lshl_add_u64 v[2:3], v[6:7], 2, v[2:3]
	global_load_dwordx4 v[6:9], v[4:5], off nt
	s_nop 0
	global_load_dwordx4 v[2:5], v[2:3], off nt
	v_lshlrev_b32_e32 v45, 3, v130
	v_and_b32_e32 v66, 56, v45
	s_movk_i32 s0, 0x404
	v_mad_u32_u24 v55, v66, s0, 0
	v_mul_lo_u32 v57, v1, s0
	v_mul_lo_u32 v58, v38, s0
	v_mul_lo_u32 v59, v39, s0
	v_mul_lo_u32 v60, v40, s0
	v_mul_lo_u32 v61, v41, s0
	v_mul_lo_u32 v62, v42, s0
	v_mul_lo_u32 v63, v43, s0
	v_mul_lo_u32 v64, v44, s0
	s_add_u32 s0, s6, 0x1e940000
	s_addc_u32 s9, s7, 0
	s_add_u32 s12, s6, 0x16940000
	s_addc_u32 s13, s7, 0
	s_add_u32 s14, s6, 0x16140000
	s_addc_u32 s15, s7, 0
	s_add_u32 s30, s6, 0x15540000
	s_addc_u32 s31, s7, 0
	s_add_u32 s6, s6, 0x11f40000
	v_add_u32_e32 v34, 0, v34
	v_ashrrev_i32_e32 v45, 3, v130
	v_ashrrev_i32_e32 v48, 3, v37
	v_ashrrev_i32_e32 v51, 3, v51
	v_ashrrev_i32_e32 v54, 3, v54
	s_addc_u32 s7, s7, 0
	s_add_i32 s10, s33, s38
	s_mov_b32 s11, 0
	v_lshl_add_u32 v46, v45, 2, v55
	v_and_b32_e32 v47, 15, v45
	v_lshl_add_u32 v49, v48, 2, v55
	v_and_b32_e32 v50, 15, v48
	v_lshl_add_u32 v52, v51, 2, v55
	v_and_b32_e32 v53, 15, v51
	v_lshl_add_u32 v55, v54, 2, v55
	v_and_b32_e32 v56, 15, v54
	s_add_i32 s34, s10, 0xfffff5c0
	s_add_i32 s35, s10, 0xfffff6c0
	v_add_u32_e32 v57, v34, v57
	v_add_u32_e32 v58, v34, v58
	v_add_u32_e32 v59, v34, v59
	v_add_u32_e32 v60, v34, v60
	v_add_u32_e32 v61, v34, v61
	v_add_u32_e32 v62, v34, v62
	v_add_u32_e32 v63, v34, v63
	v_add_u32_e32 v64, v34, v64
	v_lshlrev_b32_e32 v34, 2, v36
	v_lshlrev_b32_e32 v36, 1, v66
	s_movk_i32 s36, 0x7fff
	v_mov_b32_e32 v65, 1
	s_mov_b32 s26, s17
	s_mov_b32 s27, s29
	s_mov_b64 s[20:21], s[2:3]
	s_branch .LBB0_222

.LBB0_220:
	s_lshr_b32 s22, s39, 8
	v_cvt_f32_u32_e32 v2, s22
	s_sub_i32 s41, 0, s22
	s_abs_i32 s23, s40
	s_ashr_i32 s10, s40, 31
	v_rcp_iflag_f32_e32 v2, v2
	s_nop 0
	v_mul_f32_e32 v2, 0x4f7ffffe, v2
	v_cvt_u32_f32_e32 v2, v2
	s_nop 0
	v_readfirstlane_b32 s42, v2
	s_mul_i32 s41, s41, s42
	s_mul_hi_u32 s41, s42, s41
	s_add_i32 s42, s42, s41
	s_mul_hi_u32 s41, s23, s42
	s_mul_i32 s42, s41, s22
	s_sub_i32 s23, s23, s42
	s_add_i32 s43, s41, 1
	s_sub_i32 s42, s23, s22
	s_cmp_ge_u32 s23, s22
	s_cselect_b32 s41, s43, s41
	s_cselect_b32 s23, s42, s23
	s_add_i32 s42, s41, 1
	s_cmp_ge_u32 s23, s22
	s_cselect_b32 s23, s42, s41
	s_xor_b32 s23, s23, s10
	s_sub_i32 s23, s23, s10
	s_lshl_b32 s10, s23, 6
	s_mul_i32 s23, s23, s22
	s_sub_i32 s22, s40, s23
	s_lshl_b32 s22, s22, 8
	s_ashr_i32 s23, s22, 31
	s_lshl_b64 s[40:41], s[22:23], 2
	s_add_u32 s24, s24, s40
	v_add_u32_e32 v2, s10, v1
	s_addc_u32 s25, s25, s41
	v_add_u32_e32 v10, s10, v39
	v_add_u32_e32 v18, s10, v41
	v_add_u32_e32 v28, s10, v43
	v_ashrrev_i32_e32 v5, 31, v2
	v_lshl_add_u64 v[26:27], s[24:25], 0, v[34:35]
	v_mad_u64_u32 v[2:3], s[24:25], v2, s39, 0
	v_ashrrev_i32_e32 v13, 31, v10
	v_mad_u64_u32 v[10:11], s[24:25], v10, s39, 0
	v_ashrrev_i32_e32 v21, 31, v18
	v_mad_u64_u32 v[18:19], s[24:25], v18, s39, 0
	v_ashrrev_i32_e32 v31, 31, v28
	v_mad_u64_u32 v[28:29], s[24:25], v28, s39, 0
	v_mov_b32_e32 v4, v3
	v_mov_b32_e32 v12, v11
	v_mov_b32_e32 v20, v19
	v_mov_b32_e32 v30, v29
	v_mad_u64_u32 v[4:5], s[24:25], v5, s39, v[4:5]
	v_mad_u64_u32 v[12:13], s[24:25], v13, s39, v[12:13]
	v_mad_u64_u32 v[20:21], s[24:25], v21, s39, v[20:21]
	v_mad_u64_u32 v[30:31], s[24:25], v31, s39, v[30:31]
	v_mov_b32_e32 v3, v4
	v_add_u32_e32 v4, s10, v38
	v_mov_b32_e32 v11, v12
	v_add_u32_e32 v12, s10, v40
	v_mov_b32_e32 v19, v20
	v_add_u32_e32 v20, s10, v42
	v_mov_b32_e32 v29, v30
	v_add_u32_e32 v30, s10, v44
	v_ashrrev_i32_e32 v7, 31, v4
	v_mad_u64_u32 v[4:5], s[24:25], v4, s39, 0
	v_ashrrev_i32_e32 v15, 31, v12
	v_mad_u64_u32 v[12:13], s[24:25], v12, s39, 0
	v_ashrrev_i32_e32 v23, 31, v20
	v_mad_u64_u32 v[20:21], s[24:25], v20, s39, 0
	v_ashrrev_i32_e32 v33, 31, v30
	v_mad_u64_u32 v[30:31], s[24:25], v30, s39, 0
	v_mov_b32_e32 v6, v5
	v_mov_b32_e32 v14, v13
	v_mov_b32_e32 v22, v21
	v_mov_b32_e32 v32, v31
	v_mad_u64_u32 v[6:7], s[24:25], v7, s39, v[6:7]
	v_mad_u64_u32 v[14:15], s[24:25], v15, s39, v[14:15]
	v_mad_u64_u32 v[22:23], s[24:25], v23, s39, v[22:23]
	v_mad_u64_u32 v[32:33], s[24:25], v33, s39, v[32:33]
	v_mov_b32_e32 v5, v6
	v_mov_b32_e32 v13, v14
	v_mov_b32_e32 v21, v22
	v_mov_b32_e32 v31, v32
	v_lshl_add_u64 v[2:3], v[2:3], 2, v[26:27]
	v_lshl_add_u64 v[6:7], v[4:5], 2, v[26:27]
	v_lshl_add_u64 v[10:11], v[10:11], 2, v[26:27]
	v_lshl_add_u64 v[14:15], v[12:13], 2, v[26:27]
	v_lshl_add_u64 v[18:19], v[18:19], 2, v[26:27]
	v_lshl_add_u64 v[22:23], v[20:21], 2, v[26:27]
	v_lshl_add_u64 v[28:29], v[28:29], 2, v[26:27]
	v_lshl_add_u64 v[30:31], v[30:31], 2, v[26:27]
	global_load_dwordx4 v[2:5], v[2:3], off nt
	s_nop 0
	global_load_dwordx4 v[6:9], v[6:7], off nt
	s_nop 0
	global_load_dwordx4 v[10:13], v[10:11], off nt
	s_nop 0
	global_load_dwordx4 v[14:17], v[14:15], off nt
	s_nop 0
	global_load_dwordx4 v[18:21], v[18:19], off nt
	s_nop 0
	global_load_dwordx4 v[22:25], v[22:23], off nt
	s_nop 0
	global_load_dwordx4 v[26:29], v[28:29], off nt
	s_nop 0
	global_load_dwordx4 v[30:33], v[30:31], off nt
.LBB0_221:
	s_add_i32 s28, s28, -1
	s_cmp_eq_u32 s17, 0
	v_add_u32_e32 v66, s8, v45
	v_lshlrev_b32_e32 v37, 1, v66
	s_cselect_b64 vcc, -1, 0
	s_ashr_i32 s17, s16, 31
	v_and_b32_e32 v37, 0xffffffe0, v37
	s_lshl_b64 s[16:17], s[16:17], 1
	v_add3_u32 v67, s1, v47, v37
	s_add_u32 s2, s2, s16
	s_addc_u32 s3, s3, s17
	v_mov_b32_e32 v37, v35
	v_cndmask_b32_e32 v66, v67, v66, vcc
	v_lshl_add_u64 v[70:71], s[2:3], 0, v[36:37]
	v_ashrrev_i32_e32 v69, 31, v66
	v_mad_u64_u32 v[66:67], s[2:3], v66, s29, 0
	v_mov_b32_e32 v68, v67
	ds_read_b32 v37, v46
	ds_read_b32 v74, v46 offset:1028
	ds_read_b32 v75, v46 offset:2056
	ds_read_b32 v76, v46 offset:3084
	ds_read_b32 v77, v46 offset:4112
	ds_read_b32 v78, v46 offset:5140
	ds_read_b32 v79, v46 offset:6168
	ds_read_b32 v80, v46 offset:7196
	v_mad_u64_u32 v[68:69], s[2:3], v69, s29, v[68:69]
	v_mov_b32_e32 v67, v68
	v_lshl_add_u64 v[72:73], v[66:67], 1, v[70:71]
	s_waitcnt lgkmcnt(7)
	v_and_b32_sdwa v67, v37, v65 dst_sel:DWORD dst_unused:UNUSED_PAD src0_sel:WORD_1 src1_sel:DWORD
	v_add3_u32 v37, v37, v67, s36
	s_waitcnt lgkmcnt(4)
	v_and_b32_sdwa v67, v76, v65 dst_sel:DWORD dst_unused:UNUSED_PAD src0_sel:WORD_1 src1_sel:DWORD
	v_and_b32_sdwa v68, v74, v65 dst_sel:DWORD dst_unused:UNUSED_PAD src0_sel:WORD_1 src1_sel:DWORD
	v_and_b32_sdwa v66, v75, v65 dst_sel:DWORD dst_unused:UNUSED_PAD src0_sel:WORD_1 src1_sel:DWORD
	v_add3_u32 v67, v76, v67, s36
	v_add3_u32 v68, v74, v68, s36
	v_add3_u32 v66, v75, v66, s36
	v_and_b32_e32 v67, 0xffff0000, v67
	v_and_b32_e32 v68, 0xffff0000, v68
	s_waitcnt lgkmcnt(0)
	v_and_b32_sdwa v69, v80, v65 dst_sel:DWORD dst_unused:UNUSED_PAD src0_sel:WORD_1 src1_sel:DWORD
	v_and_b32_sdwa v74, v78, v65 dst_sel:DWORD dst_unused:UNUSED_PAD src0_sel:WORD_1 src1_sel:DWORD
	v_or_b32_sdwa v67, v67, v66 dst_sel:DWORD dst_unused:UNUSED_PAD src0_sel:DWORD src1_sel:WORD_1
	v_or_b32_sdwa v66, v68, v37 dst_sel:DWORD dst_unused:UNUSED_PAD src0_sel:DWORD src1_sel:WORD_1
	v_and_b32_sdwa v37, v79, v65 dst_sel:DWORD dst_unused:UNUSED_PAD src0_sel:WORD_1 src1_sel:DWORD
	v_and_b32_sdwa v68, v77, v65 dst_sel:DWORD dst_unused:UNUSED_PAD src0_sel:WORD_1 src1_sel:DWORD
	v_add3_u32 v69, v80, v69, s36
	v_add3_u32 v74, v78, v74, s36
	v_add3_u32 v68, v77, v68, s36
	v_add3_u32 v37, v79, v37, s36
	v_and_b32_e32 v69, 0xffff0000, v69
	v_and_b32_e32 v74, 0xffff0000, v74
	v_or_b32_sdwa v69, v69, v37 dst_sel:DWORD dst_unused:UNUSED_PAD src0_sel:DWORD src1_sel:WORD_1
	v_or_b32_sdwa v68, v74, v68 dst_sel:DWORD dst_unused:UNUSED_PAD src0_sel:DWORD src1_sel:WORD_1
	global_store_dwordx4 v[72:73], v[66:69], off nt
	ds_read_b32 v37, v49
	ds_read_b32 v74, v49 offset:1028
	ds_read_b32 v75, v49 offset:2056
	ds_read_b32 v76, v49 offset:3084
	ds_read_b32 v77, v49 offset:4112
	ds_read_b32 v78, v49 offset:5140
	ds_read_b32 v79, v49 offset:6168
	ds_read_b32 v80, v49 offset:7196
	v_add_u32_e32 v66, s8, v48
	v_lshlrev_b32_e32 v67, 1, v66
	v_and_b32_e32 v67, 0xffffffe0, v67
	v_add3_u32 v67, s1, v50, v67
	v_cndmask_b32_e32 v66, v67, v66, vcc
	v_ashrrev_i32_e32 v69, 31, v66
	v_mad_u64_u32 v[66:67], s[2:3], v66, s29, 0
	v_mov_b32_e32 v68, v67
	v_mad_u64_u32 v[68:69], s[2:3], v69, s29, v[68:69]
	v_mov_b32_e32 v67, v68
	v_lshl_add_u64 v[72:73], v[66:67], 1, v[70:71]
	s_waitcnt lgkmcnt(7)
	v_and_b32_sdwa v67, v37, v65 dst_sel:DWORD dst_unused:UNUSED_PAD src0_sel:WORD_1 src1_sel:DWORD
	v_add3_u32 v37, v37, v67, s36
	s_waitcnt lgkmcnt(4)
	v_and_b32_sdwa v67, v76, v65 dst_sel:DWORD dst_unused:UNUSED_PAD src0_sel:WORD_1 src1_sel:DWORD
	v_and_b32_sdwa v68, v74, v65 dst_sel:DWORD dst_unused:UNUSED_PAD src0_sel:WORD_1 src1_sel:DWORD
	v_and_b32_sdwa v66, v75, v65 dst_sel:DWORD dst_unused:UNUSED_PAD src0_sel:WORD_1 src1_sel:DWORD
	v_add3_u32 v67, v76, v67, s36
	v_add3_u32 v68, v74, v68, s36
	v_add3_u32 v66, v75, v66, s36
	v_and_b32_e32 v67, 0xffff0000, v67
	v_and_b32_e32 v68, 0xffff0000, v68
	s_waitcnt lgkmcnt(0)
	v_and_b32_sdwa v69, v80, v65 dst_sel:DWORD dst_unused:UNUSED_PAD src0_sel:WORD_1 src1_sel:DWORD
	v_and_b32_sdwa v74, v78, v65 dst_sel:DWORD dst_unused:UNUSED_PAD src0_sel:WORD_1 src1_sel:DWORD
	v_or_b32_sdwa v67, v67, v66 dst_sel:DWORD dst_unused:UNUSED_PAD src0_sel:DWORD src1_sel:WORD_1
	v_or_b32_sdwa v66, v68, v37 dst_sel:DWORD dst_unused:UNUSED_PAD src0_sel:DWORD src1_sel:WORD_1
	v_and_b32_sdwa v37, v79, v65 dst_sel:DWORD dst_unused:UNUSED_PAD src0_sel:WORD_1 src1_sel:DWORD
	v_and_b32_sdwa v68, v77, v65 dst_sel:DWORD dst_unused:UNUSED_PAD src0_sel:WORD_1 src1_sel:DWORD
	v_add3_u32 v69, v80, v69, s36
	v_add3_u32 v74, v78, v74, s36
	v_add3_u32 v68, v77, v68, s36
	v_add3_u32 v37, v79, v37, s36
	v_and_b32_e32 v69, 0xffff0000, v69
	v_and_b32_e32 v74, 0xffff0000, v74
	v_or_b32_sdwa v69, v69, v37 dst_sel:DWORD dst_unused:UNUSED_PAD src0_sel:DWORD src1_sel:WORD_1
	v_or_b32_sdwa v68, v74, v68 dst_sel:DWORD dst_unused:UNUSED_PAD src0_sel:DWORD src1_sel:WORD_1
	global_store_dwordx4 v[72:73], v[66:69], off nt
	ds_read_b32 v37, v52
	ds_read_b32 v74, v52 offset:1028
	ds_read_b32 v75, v52 offset:2056
	ds_read_b32 v76, v52 offset:3084
	ds_read_b32 v77, v52 offset:4112
	ds_read_b32 v78, v52 offset:5140
	ds_read_b32 v79, v52 offset:6168
	ds_read_b32 v80, v52 offset:7196
	v_add_u32_e32 v66, s8, v51
	v_lshlrev_b32_e32 v67, 1, v66
	v_and_b32_e32 v67, 0xffffffe0, v67
	v_add3_u32 v67, s1, v53, v67
	v_cndmask_b32_e32 v66, v67, v66, vcc
	v_ashrrev_i32_e32 v69, 31, v66
	v_mad_u64_u32 v[66:67], s[2:3], v66, s29, 0
	v_mov_b32_e32 v68, v67
	v_mad_u64_u32 v[68:69], s[2:3], v69, s29, v[68:69]
	v_mov_b32_e32 v67, v68
	v_lshl_add_u64 v[72:73], v[66:67], 1, v[70:71]
	s_waitcnt lgkmcnt(7)
	v_and_b32_sdwa v67, v37, v65 dst_sel:DWORD dst_unused:UNUSED_PAD src0_sel:WORD_1 src1_sel:DWORD
	v_add3_u32 v37, v37, v67, s36
	s_waitcnt lgkmcnt(4)
	v_and_b32_sdwa v67, v76, v65 dst_sel:DWORD dst_unused:UNUSED_PAD src0_sel:WORD_1 src1_sel:DWORD
	v_and_b32_sdwa v68, v74, v65 dst_sel:DWORD dst_unused:UNUSED_PAD src0_sel:WORD_1 src1_sel:DWORD
	v_and_b32_sdwa v66, v75, v65 dst_sel:DWORD dst_unused:UNUSED_PAD src0_sel:WORD_1 src1_sel:DWORD
	v_add3_u32 v67, v76, v67, s36
	v_add3_u32 v68, v74, v68, s36
	v_add3_u32 v66, v75, v66, s36
	v_and_b32_e32 v67, 0xffff0000, v67
	v_and_b32_e32 v68, 0xffff0000, v68
	s_waitcnt lgkmcnt(0)
	v_and_b32_sdwa v69, v80, v65 dst_sel:DWORD dst_unused:UNUSED_PAD src0_sel:WORD_1 src1_sel:DWORD
	v_and_b32_sdwa v74, v78, v65 dst_sel:DWORD dst_unused:UNUSED_PAD src0_sel:WORD_1 src1_sel:DWORD
	v_or_b32_sdwa v67, v67, v66 dst_sel:DWORD dst_unused:UNUSED_PAD src0_sel:DWORD src1_sel:WORD_1
	v_or_b32_sdwa v66, v68, v37 dst_sel:DWORD dst_unused:UNUSED_PAD src0_sel:DWORD src1_sel:WORD_1
	v_and_b32_sdwa v37, v79, v65 dst_sel:DWORD dst_unused:UNUSED_PAD src0_sel:WORD_1 src1_sel:DWORD
	v_and_b32_sdwa v68, v77, v65 dst_sel:DWORD dst_unused:UNUSED_PAD src0_sel:WORD_1 src1_sel:DWORD
	v_add3_u32 v69, v80, v69, s36
	v_add3_u32 v74, v78, v74, s36
	v_add3_u32 v68, v77, v68, s36
	v_add3_u32 v37, v79, v37, s36
	v_and_b32_e32 v69, 0xffff0000, v69
	v_and_b32_e32 v74, 0xffff0000, v74
	v_or_b32_sdwa v69, v69, v37 dst_sel:DWORD dst_unused:UNUSED_PAD src0_sel:DWORD src1_sel:WORD_1
	v_or_b32_sdwa v68, v74, v68 dst_sel:DWORD dst_unused:UNUSED_PAD src0_sel:DWORD src1_sel:WORD_1
	global_store_dwordx4 v[72:73], v[66:69], off nt
	ds_read_b32 v37, v55
	ds_read_b32 v72, v55 offset:1028
	ds_read_b32 v73, v55 offset:2056
	ds_read_b32 v74, v55 offset:3084
	ds_read_b32 v75, v55 offset:4112
	ds_read_b32 v76, v55 offset:5140
	ds_read_b32 v77, v55 offset:6168
	ds_read_b32 v78, v55 offset:7196
	v_add_u32_e32 v66, s8, v54
	v_lshlrev_b32_e32 v67, 1, v66
	v_and_b32_e32 v67, 0xffffffe0, v67
	v_add3_u32 v67, s1, v56, v67
	v_cndmask_b32_e32 v66, v67, v66, vcc
	v_ashrrev_i32_e32 v69, 31, v66
	v_mad_u64_u32 v[66:67], s[2:3], v66, s29, 0
	v_mov_b32_e32 v68, v67
	v_mad_u64_u32 v[68:69], s[2:3], v69, s29, v[68:69]
	v_mov_b32_e32 v67, v68
	v_lshl_add_u64 v[70:71], v[66:67], 1, v[70:71]
	s_waitcnt lgkmcnt(7)
	v_and_b32_sdwa v67, v37, v65 dst_sel:DWORD dst_unused:UNUSED_PAD src0_sel:WORD_1 src1_sel:DWORD
	v_add3_u32 v37, v37, v67, s36
	s_waitcnt lgkmcnt(4)
	v_and_b32_sdwa v67, v74, v65 dst_sel:DWORD dst_unused:UNUSED_PAD src0_sel:WORD_1 src1_sel:DWORD
	v_and_b32_sdwa v68, v72, v65 dst_sel:DWORD dst_unused:UNUSED_PAD src0_sel:WORD_1 src1_sel:DWORD
	v_and_b32_sdwa v66, v73, v65 dst_sel:DWORD dst_unused:UNUSED_PAD src0_sel:WORD_1 src1_sel:DWORD
	v_add3_u32 v67, v74, v67, s36
	v_add3_u32 v68, v72, v68, s36
	v_add3_u32 v66, v73, v66, s36
	v_and_b32_e32 v67, 0xffff0000, v67
	v_and_b32_e32 v68, 0xffff0000, v68
	s_waitcnt lgkmcnt(0)
	v_and_b32_sdwa v69, v78, v65 dst_sel:DWORD dst_unused:UNUSED_PAD src0_sel:WORD_1 src1_sel:DWORD
	v_and_b32_sdwa v72, v76, v65 dst_sel:DWORD dst_unused:UNUSED_PAD src0_sel:WORD_1 src1_sel:DWORD
	v_or_b32_sdwa v67, v67, v66 dst_sel:DWORD dst_unused:UNUSED_PAD src0_sel:DWORD src1_sel:WORD_1
	v_or_b32_sdwa v66, v68, v37 dst_sel:DWORD dst_unused:UNUSED_PAD src0_sel:DWORD src1_sel:WORD_1
	v_and_b32_sdwa v37, v77, v65 dst_sel:DWORD dst_unused:UNUSED_PAD src0_sel:WORD_1 src1_sel:DWORD
	v_and_b32_sdwa v68, v75, v65 dst_sel:DWORD dst_unused:UNUSED_PAD src0_sel:WORD_1 src1_sel:DWORD
	v_add3_u32 v69, v78, v69, s36
	v_add3_u32 v72, v76, v72, s36
	v_add3_u32 v68, v75, v68, s36
	v_add3_u32 v37, v77, v37, s36
	v_and_b32_e32 v69, 0xffff0000, v69
	v_and_b32_e32 v72, 0xffff0000, v72
	v_or_b32_sdwa v69, v69, v37 dst_sel:DWORD dst_unused:UNUSED_PAD src0_sel:DWORD src1_sel:WORD_1
	v_or_b32_sdwa v68, v72, v68 dst_sel:DWORD dst_unused:UNUSED_PAD src0_sel:DWORD src1_sel:WORD_1
	s_add_i32 s34, s34, s38
	s_add_i32 s35, s35, s38
	s_andn2_b64 vcc, exec, s[18:19]
	s_mov_b32 s1, s37
	s_mov_b32 s17, s26
	s_mov_b32 s8, s22
	s_mov_b32 s16, s10
	s_mov_b32 s29, s27
	s_mov_b64 s[2:3], s[20:21]
	global_store_dwordx4 v[70:71], v[66:69], off nt
	s_barrier
	s_cbranch_vccz .LBB0_240

.LBB0_1942:
	s_waitcnt vmcnt(11)
	v_add_u32_e32 v2, 0x800, v34
	s_lshr_b32 s4, s8, 8
	v_ashrrev_i32_e32 v42, 6, v2
	v_cvt_f32_u32_e32 v2, s4
	s_sub_i32 s11, 0, s4
	s_abs_i32 s10, s9
	s_ashr_i32 s5, s9, 31
	v_rcp_iflag_f32_e32 v2, v2
	v_add_u32_e32 v3, 0xa00, v34
	v_ashrrev_i32_e32 v43, 6, v3
	v_add_u32_e32 v3, 0xc00, v34
	v_mul_f32_e32 v2, 0x4f7ffffe, v2
	v_cvt_u32_f32_e32 v2, v2
	v_lshlrev_b32_e32 v1, 2, v34
	v_ashrrev_i32_e32 v44, 6, v3
	v_add_u32_e32 v3, 0xe00, v34
	v_readfirstlane_b32 s12, v2
	s_mul_i32 s11, s11, s12
	s_mul_hi_u32 s11, s12, s11
	s_add_i32 s12, s12, s11
	s_mul_hi_u32 s11, s10, s12
	s_mul_i32 s12, s11, s4
	s_sub_i32 s10, s10, s12
	s_add_i32 s12, s11, 1
	s_sub_i32 s13, s10, s4
	s_cmp_ge_u32 s10, s4
	s_cselect_b32 s11, s12, s11
	s_cselect_b32 s10, s13, s10
	s_add_i32 s12, s11, 1
	s_cmp_ge_u32 s10, s4
	s_cselect_b32 s10, s12, s11
	s_xor_b32 s10, s10, s5
	s_sub_i32 s12, s10, s5
	s_mul_i32 s4, s12, s4
	s_sub_i32 s4, s9, s4
	s_lshl_b32 s4, s4, 8
	s_ashr_i32 s5, s4, 31
	s_lshl_b64 s[10:11], s[4:5], 2
	s_add_u32 s6, s6, s10
	v_and_b32_e32 v38, 0xfc, v1
	v_ashrrev_i32_e32 v45, 6, v3
	s_addc_u32 s7, s7, s11
	s_lshl_b32 s14, s12, 6
	v_mov_b32_e32 v37, 0
	v_lshlrev_b32_e32 v36, 2, v38
	v_add_u32_e32 v4, s14, v45
	v_lshl_add_u64 v[2:3], s[6:7], 0, v[36:37]
	s_waitcnt vmcnt(10)
	v_ashrrev_i32_e32 v7, 31, v4
	v_mad_u64_u32 v[4:5], s[6:7], v4, s8, 0
	v_mov_b32_e32 v6, v5
	v_mad_u64_u32 v[6:7], s[6:7], v7, s8, v[6:7]
	v_mov_b32_e32 v5, v6
	v_add_u32_e32 v6, s14, v44
	v_ashrrev_i32_e32 v9, 31, v6
	v_mad_u64_u32 v[6:7], s[6:7], v6, s8, 0
	v_mov_b32_e32 v8, v7
	v_mad_u64_u32 v[8:9], s[6:7], v9, s8, v[8:9]
	v_lshl_add_u64 v[4:5], v[4:5], 2, v[2:3]
	v_mov_b32_e32 v7, v8
	v_lshl_add_u64 v[6:7], v[6:7], 2, v[2:3]
	global_load_dwordx4 v[30:33], v[4:5], off nt
	global_load_dwordx4 v[26:29], v[6:7], off nt
	v_add_u32_e32 v4, s14, v43
	v_ashrrev_i32_e32 v7, 31, v4
	v_mad_u64_u32 v[4:5], s[6:7], v4, s8, 0
	v_mov_b32_e32 v6, v5
	v_mad_u64_u32 v[6:7], s[6:7], v7, s8, v[6:7]
	v_mov_b32_e32 v5, v6
	v_add_u32_e32 v6, s14, v42
	v_ashrrev_i32_e32 v9, 31, v6
	v_mad_u64_u32 v[6:7], s[6:7], v6, s8, 0
	v_mov_b32_e32 v8, v7
	v_add_u32_e32 v55, 0x600, v34
	v_mad_u64_u32 v[8:9], s[6:7], v9, s8, v[8:9]
	v_ashrrev_i32_e32 v41, 6, v55
	v_lshl_add_u64 v[4:5], v[4:5], 2, v[2:3]
	v_mov_b32_e32 v7, v8
	v_lshl_add_u64 v[6:7], v[6:7], 2, v[2:3]
	global_load_dwordx4 v[22:25], v[4:5], off nt
	global_load_dwordx4 v[18:21], v[6:7], off nt
	v_add_u32_e32 v4, s14, v41
	v_ashrrev_i32_e32 v7, 31, v4
	v_mad_u64_u32 v[4:5], s[6:7], v4, s8, 0
	v_add_u32_e32 v52, 0x400, v34
	v_mov_b32_e32 v6, v5
	v_ashrrev_i32_e32 v40, 6, v52
	v_mad_u64_u32 v[6:7], s[6:7], v7, s8, v[6:7]
	v_mov_b32_e32 v5, v6
	v_add_u32_e32 v6, s14, v40
	v_ashrrev_i32_e32 v9, 31, v6
	v_mad_u64_u32 v[6:7], s[6:7], v6, s8, 0
	v_mov_b32_e32 v8, v7
	v_add_u32_e32 v39, 0x200, v34
	v_mad_u64_u32 v[8:9], s[6:7], v9, s8, v[8:9]
	v_ashrrev_i32_e32 v35, 6, v39
	v_lshl_add_u64 v[4:5], v[4:5], 2, v[2:3]
	v_mov_b32_e32 v7, v8
	v_lshl_add_u64 v[6:7], v[6:7], 2, v[2:3]
	global_load_dwordx4 v[14:17], v[4:5], off nt
	global_load_dwordx4 v[10:13], v[6:7], off nt
	v_add_u32_e32 v4, s14, v35
	v_ashrrev_i32_e32 v7, 31, v4
	v_mad_u64_u32 v[4:5], s[6:7], v4, s8, 0
	v_mov_b32_e32 v6, v5
	v_ashrrev_i32_e32 v1, 6, v34
	v_mad_u64_u32 v[6:7], s[6:7], v7, s8, v[6:7]
	v_mov_b32_e32 v5, v6
	v_add_u32_e32 v6, s14, v1
	v_ashrrev_i32_e32 v9, 31, v6
	v_mad_u64_u32 v[6:7], s[6:7], v6, s8, 0
	v_mov_b32_e32 v8, v7
	v_mad_u64_u32 v[8:9], s[6:7], v9, s8, v[8:9]
	v_mov_b32_e32 v7, v8
	v_lshl_add_u64 v[4:5], v[4:5], 2, v[2:3]
	v_lshl_add_u64 v[2:3], v[6:7], 2, v[2:3]
	global_load_dwordx4 v[6:9], v[4:5], off nt
	s_nop 0
	global_load_dwordx4 v[2:5], v[2:3], off nt
	v_lshlrev_b32_e32 v46, 3, v34
	v_and_b32_e32 v66, 56, v46
	s_movk_i32 s5, 0x404
	v_readlane_b32 s12, v251, 60
	v_mad_u32_u24 v56, v66, s5, 0
	v_mul_lo_u32 v58, v1, s5
	v_mul_lo_u32 v59, v35, s5
	v_mul_lo_u32 v60, v40, s5
	v_mul_lo_u32 v61, v41, s5
	v_mul_lo_u32 v62, v42, s5
	v_mul_lo_u32 v63, v43, s5
	v_mul_lo_u32 v64, v44, s5
	v_mul_lo_u32 v65, v45, s5
	v_readlane_b32 s13, v251, 61
	s_add_u32 s5, s12, 0x1e940000
	s_addc_u32 s26, s13, 0
	s_add_u32 s8, s12, 0x16940000
	s_addc_u32 s9, s13, 0
	s_add_u32 s10, s12, 0x16140000
	s_addc_u32 s11, s13, 0
	s_add_u32 s27, s12, 0x15540000
	s_addc_u32 s28, s13, 0
	v_add_u32_e32 v36, 0, v36
	v_ashrrev_i32_e32 v46, 3, v34
	v_ashrrev_i32_e32 v49, 3, v39
	v_ashrrev_i32_e32 v52, 3, v52
	v_ashrrev_i32_e32 v55, 3, v55
	s_add_u32 s12, s12, 0x11f40000
	s_mov_b32 s7, 0
	v_lshl_add_u32 v47, v46, 2, v56
	v_and_b32_e32 v48, 15, v46
	v_lshl_add_u32 v50, v49, 2, v56
	v_and_b32_e32 v51, 15, v49
	v_lshl_add_u32 v53, v52, 2, v56
	v_and_b32_e32 v54, 15, v52
	v_lshl_add_u32 v56, v55, 2, v56
	v_and_b32_e32 v57, 15, v55
	s_addc_u32 s13, s13, 0
	s_add_i32 s29, s16, 0x15e1
	s_mov_b32 s30, 17
	v_add_u32_e32 v58, v36, v58
	v_add_u32_e32 v59, v36, v59
	v_add_u32_e32 v60, v36, v60
	v_add_u32_e32 v61, v36, v61
	v_add_u32_e32 v62, v36, v62
	v_add_u32_e32 v63, v36, v63
	v_add_u32_e32 v64, v36, v64
	v_add_u32_e32 v65, v36, v65
	v_lshlrev_b32_e32 v36, 2, v38
	v_lshlrev_b32_e32 v38, 1, v66
	s_movk_i32 s31, 0x7fff
	v_mov_b32_e32 v66, 1
	s_mov_b32 s24, s15
	s_mov_b32 s25, s0
	s_mov_b64 s[18:19], s[2:3]
	v_readlane_b32 s42, v251, 58
	v_readlane_b32 s43, v251, 59
	s_branch .LBB0_1946

.LBB0_1944:
	s_lshr_b32 s20, s36, 8
	v_cvt_f32_u32_e32 v2, s20
	s_sub_i32 s34, 0, s20
	s_abs_i32 s21, s37
	s_ashr_i32 s6, s37, 31
	v_rcp_iflag_f32_e32 v2, v2
	s_nop 0
	v_mul_f32_e32 v2, 0x4f7ffffe, v2
	v_cvt_u32_f32_e32 v2, v2
	s_nop 0
	v_readfirstlane_b32 s38, v2
	s_mul_i32 s34, s34, s38
	s_mul_hi_u32 s34, s38, s34
	s_add_i32 s38, s38, s34
	s_mul_hi_u32 s34, s21, s38
	s_mul_i32 s38, s34, s20
	s_sub_i32 s21, s21, s38
	s_add_i32 s39, s34, 1
	s_sub_i32 s38, s21, s20
	s_cmp_ge_u32 s21, s20
	s_cselect_b32 s34, s39, s34
	s_cselect_b32 s21, s38, s21
	s_add_i32 s38, s34, 1
	s_cmp_ge_u32 s21, s20
	s_cselect_b32 s21, s38, s34
	s_xor_b32 s21, s21, s6
	s_sub_i32 s21, s21, s6
	s_lshl_b32 s6, s21, 6
	s_mul_i32 s21, s21, s20
	s_sub_i32 s20, s37, s21
	s_lshl_b32 s20, s20, 8
	s_ashr_i32 s21, s20, 31
	s_lshl_b64 s[38:39], s[20:21], 2
	s_add_u32 s22, s22, s38
	v_add_u32_e32 v2, s6, v1
	s_addc_u32 s23, s23, s39
	v_add_u32_e32 v10, s6, v40
	v_add_u32_e32 v18, s6, v42
	v_add_u32_e32 v28, s6, v44
	v_ashrrev_i32_e32 v5, 31, v2
	v_lshl_add_u64 v[26:27], s[22:23], 0, v[36:37]
	v_mad_u64_u32 v[2:3], s[22:23], v2, s36, 0
	v_ashrrev_i32_e32 v13, 31, v10
	v_mad_u64_u32 v[10:11], s[22:23], v10, s36, 0
	v_ashrrev_i32_e32 v21, 31, v18
	v_mad_u64_u32 v[18:19], s[22:23], v18, s36, 0
	v_ashrrev_i32_e32 v31, 31, v28
	v_mad_u64_u32 v[28:29], s[22:23], v28, s36, 0
	v_mov_b32_e32 v4, v3
	v_mov_b32_e32 v12, v11
	v_mov_b32_e32 v20, v19
	v_mov_b32_e32 v30, v29
	v_mad_u64_u32 v[4:5], s[22:23], v5, s36, v[4:5]
	v_mad_u64_u32 v[12:13], s[22:23], v13, s36, v[12:13]
	v_mad_u64_u32 v[20:21], s[22:23], v21, s36, v[20:21]
	v_mad_u64_u32 v[30:31], s[22:23], v31, s36, v[30:31]
	v_mov_b32_e32 v3, v4
	v_add_u32_e32 v4, s6, v35
	v_mov_b32_e32 v11, v12
	v_add_u32_e32 v12, s6, v41
	v_mov_b32_e32 v19, v20
	v_add_u32_e32 v20, s6, v43
	v_mov_b32_e32 v29, v30
	v_add_u32_e32 v30, s6, v45
	v_ashrrev_i32_e32 v7, 31, v4
	v_mad_u64_u32 v[4:5], s[22:23], v4, s36, 0
	v_ashrrev_i32_e32 v15, 31, v12
	v_mad_u64_u32 v[12:13], s[22:23], v12, s36, 0
	v_ashrrev_i32_e32 v23, 31, v20
	v_mad_u64_u32 v[20:21], s[22:23], v20, s36, 0
	v_ashrrev_i32_e32 v33, 31, v30
	v_mad_u64_u32 v[30:31], s[22:23], v30, s36, 0
	v_mov_b32_e32 v6, v5
	v_mov_b32_e32 v14, v13
	v_mov_b32_e32 v22, v21
	v_mov_b32_e32 v32, v31
	v_mad_u64_u32 v[6:7], s[22:23], v7, s36, v[6:7]
	v_mad_u64_u32 v[14:15], s[22:23], v15, s36, v[14:15]
	v_mad_u64_u32 v[22:23], s[22:23], v23, s36, v[22:23]
	v_mad_u64_u32 v[32:33], s[22:23], v33, s36, v[32:33]
	v_mov_b32_e32 v5, v6
	v_mov_b32_e32 v13, v14
	v_mov_b32_e32 v21, v22
	v_mov_b32_e32 v31, v32
	v_lshl_add_u64 v[2:3], v[2:3], 2, v[26:27]
	v_lshl_add_u64 v[6:7], v[4:5], 2, v[26:27]
	v_lshl_add_u64 v[10:11], v[10:11], 2, v[26:27]
	v_lshl_add_u64 v[14:15], v[12:13], 2, v[26:27]
	v_lshl_add_u64 v[18:19], v[18:19], 2, v[26:27]
	v_lshl_add_u64 v[22:23], v[20:21], 2, v[26:27]
	v_lshl_add_u64 v[28:29], v[28:29], 2, v[26:27]
	v_lshl_add_u64 v[30:31], v[30:31], 2, v[26:27]
	global_load_dwordx4 v[2:5], v[2:3], off nt
	s_nop 0
	global_load_dwordx4 v[6:9], v[6:7], off nt
	s_nop 0
	global_load_dwordx4 v[10:13], v[10:11], off nt
	s_nop 0
	global_load_dwordx4 v[14:17], v[14:15], off nt
	s_nop 0
	global_load_dwordx4 v[18:21], v[18:19], off nt
	s_nop 0
	global_load_dwordx4 v[22:25], v[22:23], off nt
	s_nop 0
	global_load_dwordx4 v[26:29], v[28:29], off nt
	s_nop 0
	global_load_dwordx4 v[30:33], v[30:31], off nt
.LBB0_1945:
	s_add_i32 s30, s30, -1
	s_cmp_eq_u32 s15, 0
	v_add_u32_e32 v67, s4, v46
	v_lshlrev_b32_e32 v39, 1, v67
	s_cselect_b64 vcc, -1, 0
	s_ashr_i32 s15, s14, 31
	v_and_b32_e32 v39, 0xffffffe0, v39
	s_lshl_b64 s[14:15], s[14:15], 1
	v_add3_u32 v68, s1, v48, v39
	s_add_u32 s2, s2, s14
	s_addc_u32 s3, s3, s15
	v_mov_b32_e32 v39, v37
	v_cndmask_b32_e32 v67, v68, v67, vcc
	v_lshl_add_u64 v[72:73], s[2:3], 0, v[38:39]
	v_mad_u64_u32 v[68:69], s[2:3], v67, s0, 0
	v_ashrrev_i32_e32 v71, 31, v67
	v_mov_b32_e32 v70, v69
	v_mad_u64_u32 v[70:71], s[2:3], v71, s0, v[70:71]
	ds_read_b32 v39, v47
	ds_read_b32 v76, v47 offset:1028
	ds_read_b32 v77, v47 offset:2056
	ds_read_b32 v78, v47 offset:3084
	ds_read_b32 v79, v47 offset:4112
	ds_read_b32 v80, v47 offset:5140
	ds_read_b32 v81, v47 offset:6168
	ds_read_b32 v82, v47 offset:7196
	v_mov_b32_e32 v69, v70
	v_lshl_add_u64 v[74:75], v[68:69], 1, v[72:73]
	s_waitcnt lgkmcnt(7)
	v_and_b32_sdwa v68, v39, v66 dst_sel:DWORD dst_unused:UNUSED_PAD src0_sel:WORD_1 src1_sel:DWORD
	v_add3_u32 v39, v39, v68, s31
	s_waitcnt lgkmcnt(4)
	v_and_b32_sdwa v68, v78, v66 dst_sel:DWORD dst_unused:UNUSED_PAD src0_sel:WORD_1 src1_sel:DWORD
	v_and_b32_sdwa v69, v76, v66 dst_sel:DWORD dst_unused:UNUSED_PAD src0_sel:WORD_1 src1_sel:DWORD
	v_and_b32_sdwa v67, v77, v66 dst_sel:DWORD dst_unused:UNUSED_PAD src0_sel:WORD_1 src1_sel:DWORD
	v_add3_u32 v68, v78, v68, s31
	v_add3_u32 v69, v76, v69, s31
	v_add3_u32 v67, v77, v67, s31
	v_and_b32_e32 v68, 0xffff0000, v68
	v_and_b32_e32 v70, 0xffff0000, v69
	v_or_b32_sdwa v69, v68, v67 dst_sel:DWORD dst_unused:UNUSED_PAD src0_sel:DWORD src1_sel:WORD_1
	v_or_b32_sdwa v68, v70, v39 dst_sel:DWORD dst_unused:UNUSED_PAD src0_sel:DWORD src1_sel:WORD_1
	s_waitcnt lgkmcnt(0)
	v_and_b32_sdwa v70, v82, v66 dst_sel:DWORD dst_unused:UNUSED_PAD src0_sel:WORD_1 src1_sel:DWORD
	v_and_b32_sdwa v71, v80, v66 dst_sel:DWORD dst_unused:UNUSED_PAD src0_sel:WORD_1 src1_sel:DWORD
	v_and_b32_sdwa v39, v81, v66 dst_sel:DWORD dst_unused:UNUSED_PAD src0_sel:WORD_1 src1_sel:DWORD
	v_and_b32_sdwa v67, v79, v66 dst_sel:DWORD dst_unused:UNUSED_PAD src0_sel:WORD_1 src1_sel:DWORD
	v_add3_u32 v70, v82, v70, s31
	v_add3_u32 v71, v80, v71, s31
	v_add3_u32 v67, v79, v67, s31
	v_add3_u32 v39, v81, v39, s31
	v_and_b32_e32 v70, 0xffff0000, v70
	v_and_b32_e32 v76, 0xffff0000, v71
	v_or_b32_sdwa v71, v70, v39 dst_sel:DWORD dst_unused:UNUSED_PAD src0_sel:DWORD src1_sel:WORD_1
	v_or_b32_sdwa v70, v76, v67 dst_sel:DWORD dst_unused:UNUSED_PAD src0_sel:DWORD src1_sel:WORD_1
	global_store_dwordx4 v[74:75], v[68:71], off nt
	ds_read_b32 v39, v50
	ds_read_b32 v67, v50 offset:1028
	ds_read_b32 v76, v50 offset:2056
	ds_read_b32 v77, v50 offset:3084
	ds_read_b32 v78, v50 offset:4112
	ds_read_b32 v79, v50 offset:5140
	ds_read_b32 v80, v50 offset:6168
	ds_read_b32 v81, v50 offset:7196
	v_add_u32_e32 v68, s4, v49
	v_lshlrev_b32_e32 v69, 1, v68
	v_and_b32_e32 v69, 0xffffffe0, v69
	v_add3_u32 v69, s1, v51, v69
	v_cndmask_b32_e32 v68, v69, v68, vcc
	v_ashrrev_i32_e32 v71, 31, v68
	v_mad_u64_u32 v[68:69], s[2:3], v68, s0, 0
	v_mov_b32_e32 v70, v69
	v_mad_u64_u32 v[70:71], s[2:3], v71, s0, v[70:71]
	v_mov_b32_e32 v69, v70
	v_lshl_add_u64 v[74:75], v[68:69], 1, v[72:73]
	s_waitcnt lgkmcnt(7)
	v_and_b32_sdwa v69, v39, v66 dst_sel:DWORD dst_unused:UNUSED_PAD src0_sel:WORD_1 src1_sel:DWORD
	v_add3_u32 v39, v39, v69, s31
	s_waitcnt lgkmcnt(4)
	v_and_b32_sdwa v69, v77, v66 dst_sel:DWORD dst_unused:UNUSED_PAD src0_sel:WORD_1 src1_sel:DWORD
	v_and_b32_sdwa v70, v67, v66 dst_sel:DWORD dst_unused:UNUSED_PAD src0_sel:WORD_1 src1_sel:DWORD
	v_and_b32_sdwa v68, v76, v66 dst_sel:DWORD dst_unused:UNUSED_PAD src0_sel:WORD_1 src1_sel:DWORD
	v_add3_u32 v69, v77, v69, s31
	v_add3_u32 v67, v67, v70, s31
	v_add3_u32 v68, v76, v68, s31
	v_and_b32_e32 v69, 0xffff0000, v69
	v_and_b32_e32 v67, 0xffff0000, v67
	s_waitcnt lgkmcnt(0)
	v_and_b32_sdwa v70, v81, v66 dst_sel:DWORD dst_unused:UNUSED_PAD src0_sel:WORD_1 src1_sel:DWORD
	v_and_b32_sdwa v71, v79, v66 dst_sel:DWORD dst_unused:UNUSED_PAD src0_sel:WORD_1 src1_sel:DWORD
	v_or_b32_sdwa v69, v69, v68 dst_sel:DWORD dst_unused:UNUSED_PAD src0_sel:DWORD src1_sel:WORD_1
	v_or_b32_sdwa v68, v67, v39 dst_sel:DWORD dst_unused:UNUSED_PAD src0_sel:DWORD src1_sel:WORD_1
	v_and_b32_sdwa v39, v80, v66 dst_sel:DWORD dst_unused:UNUSED_PAD src0_sel:WORD_1 src1_sel:DWORD
	v_and_b32_sdwa v67, v78, v66 dst_sel:DWORD dst_unused:UNUSED_PAD src0_sel:WORD_1 src1_sel:DWORD
	v_add3_u32 v70, v81, v70, s31
	v_add3_u32 v71, v79, v71, s31
	v_add3_u32 v67, v78, v67, s31
	v_add3_u32 v39, v80, v39, s31
	v_and_b32_e32 v70, 0xffff0000, v70
	v_and_b32_e32 v76, 0xffff0000, v71
	v_or_b32_sdwa v71, v70, v39 dst_sel:DWORD dst_unused:UNUSED_PAD src0_sel:DWORD src1_sel:WORD_1
	v_or_b32_sdwa v70, v76, v67 dst_sel:DWORD dst_unused:UNUSED_PAD src0_sel:DWORD src1_sel:WORD_1
	global_store_dwordx4 v[74:75], v[68:71], off nt
	ds_read_b32 v39, v53
	ds_read_b32 v67, v53 offset:1028
	ds_read_b32 v76, v53 offset:2056
	ds_read_b32 v77, v53 offset:3084
	ds_read_b32 v78, v53 offset:4112
	ds_read_b32 v79, v53 offset:5140
	ds_read_b32 v80, v53 offset:6168
	ds_read_b32 v81, v53 offset:7196
	v_add_u32_e32 v68, s4, v52
	v_lshlrev_b32_e32 v69, 1, v68
	v_and_b32_e32 v69, 0xffffffe0, v69
	v_add3_u32 v69, s1, v54, v69
	v_cndmask_b32_e32 v68, v69, v68, vcc
	v_ashrrev_i32_e32 v71, 31, v68
	v_mad_u64_u32 v[68:69], s[2:3], v68, s0, 0
	v_mov_b32_e32 v70, v69
	v_mad_u64_u32 v[70:71], s[2:3], v71, s0, v[70:71]
	v_mov_b32_e32 v69, v70
	v_lshl_add_u64 v[74:75], v[68:69], 1, v[72:73]
	s_waitcnt lgkmcnt(7)
	v_and_b32_sdwa v69, v39, v66 dst_sel:DWORD dst_unused:UNUSED_PAD src0_sel:WORD_1 src1_sel:DWORD
	v_add3_u32 v39, v39, v69, s31
	s_waitcnt lgkmcnt(4)
	v_and_b32_sdwa v69, v77, v66 dst_sel:DWORD dst_unused:UNUSED_PAD src0_sel:WORD_1 src1_sel:DWORD
	v_and_b32_sdwa v70, v67, v66 dst_sel:DWORD dst_unused:UNUSED_PAD src0_sel:WORD_1 src1_sel:DWORD
	v_and_b32_sdwa v68, v76, v66 dst_sel:DWORD dst_unused:UNUSED_PAD src0_sel:WORD_1 src1_sel:DWORD
	v_add3_u32 v69, v77, v69, s31
	v_add3_u32 v67, v67, v70, s31
	v_add3_u32 v68, v76, v68, s31
	v_and_b32_e32 v69, 0xffff0000, v69
	v_and_b32_e32 v67, 0xffff0000, v67
	s_waitcnt lgkmcnt(0)
	v_and_b32_sdwa v70, v81, v66 dst_sel:DWORD dst_unused:UNUSED_PAD src0_sel:WORD_1 src1_sel:DWORD
	v_and_b32_sdwa v71, v79, v66 dst_sel:DWORD dst_unused:UNUSED_PAD src0_sel:WORD_1 src1_sel:DWORD
	v_or_b32_sdwa v69, v69, v68 dst_sel:DWORD dst_unused:UNUSED_PAD src0_sel:DWORD src1_sel:WORD_1
	v_or_b32_sdwa v68, v67, v39 dst_sel:DWORD dst_unused:UNUSED_PAD src0_sel:DWORD src1_sel:WORD_1
	v_and_b32_sdwa v39, v80, v66 dst_sel:DWORD dst_unused:UNUSED_PAD src0_sel:WORD_1 src1_sel:DWORD
	v_and_b32_sdwa v67, v78, v66 dst_sel:DWORD dst_unused:UNUSED_PAD src0_sel:WORD_1 src1_sel:DWORD
	v_add3_u32 v70, v81, v70, s31
	v_add3_u32 v71, v79, v71, s31
	v_add3_u32 v67, v78, v67, s31
	v_add3_u32 v39, v80, v39, s31
	v_and_b32_e32 v70, 0xffff0000, v70
	v_and_b32_e32 v76, 0xffff0000, v71
	v_or_b32_sdwa v71, v70, v39 dst_sel:DWORD dst_unused:UNUSED_PAD src0_sel:DWORD src1_sel:WORD_1
	v_or_b32_sdwa v70, v76, v67 dst_sel:DWORD dst_unused:UNUSED_PAD src0_sel:DWORD src1_sel:WORD_1
	global_store_dwordx4 v[74:75], v[68:71], off nt
	ds_read_b32 v39, v56
	ds_read_b32 v67, v56 offset:1028
	ds_read_b32 v74, v56 offset:2056
	ds_read_b32 v75, v56 offset:3084
	ds_read_b32 v76, v56 offset:4112
	ds_read_b32 v77, v56 offset:5140
	ds_read_b32 v78, v56 offset:6168
	ds_read_b32 v79, v56 offset:7196
	v_add_u32_e32 v68, s4, v55
	v_lshlrev_b32_e32 v69, 1, v68
	v_and_b32_e32 v69, 0xffffffe0, v69
	v_add3_u32 v69, s1, v57, v69
	v_cndmask_b32_e32 v68, v69, v68, vcc
	v_ashrrev_i32_e32 v71, 31, v68
	v_mad_u64_u32 v[68:69], s[2:3], v68, s0, 0
	v_mov_b32_e32 v70, v69
	v_mad_u64_u32 v[70:71], s[0:1], v71, s0, v[70:71]
	v_mov_b32_e32 v69, v70
	v_lshl_add_u64 v[72:73], v[68:69], 1, v[72:73]
	s_waitcnt lgkmcnt(7)
	v_and_b32_sdwa v69, v39, v66 dst_sel:DWORD dst_unused:UNUSED_PAD src0_sel:WORD_1 src1_sel:DWORD
	v_add3_u32 v39, v39, v69, s31
	s_waitcnt lgkmcnt(4)
	v_and_b32_sdwa v69, v75, v66 dst_sel:DWORD dst_unused:UNUSED_PAD src0_sel:WORD_1 src1_sel:DWORD
	v_and_b32_sdwa v70, v67, v66 dst_sel:DWORD dst_unused:UNUSED_PAD src0_sel:WORD_1 src1_sel:DWORD
	v_and_b32_sdwa v68, v74, v66 dst_sel:DWORD dst_unused:UNUSED_PAD src0_sel:WORD_1 src1_sel:DWORD
	v_add3_u32 v69, v75, v69, s31
	v_add3_u32 v67, v67, v70, s31
	v_add3_u32 v68, v74, v68, s31
	v_and_b32_e32 v69, 0xffff0000, v69
	v_and_b32_e32 v67, 0xffff0000, v67
	s_waitcnt lgkmcnt(0)
	v_and_b32_sdwa v70, v79, v66 dst_sel:DWORD dst_unused:UNUSED_PAD src0_sel:WORD_1 src1_sel:DWORD
	v_and_b32_sdwa v71, v77, v66 dst_sel:DWORD dst_unused:UNUSED_PAD src0_sel:WORD_1 src1_sel:DWORD
	v_or_b32_sdwa v69, v69, v68 dst_sel:DWORD dst_unused:UNUSED_PAD src0_sel:DWORD src1_sel:WORD_1
	v_or_b32_sdwa v68, v67, v39 dst_sel:DWORD dst_unused:UNUSED_PAD src0_sel:DWORD src1_sel:WORD_1
	v_and_b32_sdwa v39, v78, v66 dst_sel:DWORD dst_unused:UNUSED_PAD src0_sel:WORD_1 src1_sel:DWORD
	v_and_b32_sdwa v67, v76, v66 dst_sel:DWORD dst_unused:UNUSED_PAD src0_sel:WORD_1 src1_sel:DWORD
	v_add3_u32 v70, v79, v70, s31
	v_add3_u32 v71, v77, v71, s31
	v_add3_u32 v67, v76, v67, s31
	v_add3_u32 v39, v78, v39, s31
	v_and_b32_e32 v70, 0xffff0000, v70
	v_and_b32_e32 v74, 0xffff0000, v71
	v_or_b32_sdwa v71, v70, v39 dst_sel:DWORD dst_unused:UNUSED_PAD src0_sel:DWORD src1_sel:WORD_1
	v_or_b32_sdwa v70, v74, v67 dst_sel:DWORD dst_unused:UNUSED_PAD src0_sel:DWORD src1_sel:WORD_1
	s_add_i32 s29, s29, 1
	s_and_b64 vcc, exec, s[16:17]
	s_mov_b32 s34, s33
	s_mov_b32 s1, s35
	s_mov_b32 s15, s24
	s_mov_b32 s4, s20
	s_mov_b32 s14, s6
	s_mov_b32 s0, s25
	s_mov_b64 s[2:3], s[18:19]
	global_store_dwordx4 v[72:73], v[68:71], off nt
	s_barrier
	s_cbranch_vccnz .LBB0_1964

.LBB0_1991:
	s_waitcnt vmcnt(11)
	v_add_u32_e32 v2, 0x800, v34
	s_lshr_b32 s0, s8, 8
	v_ashrrev_i32_e32 v42, 6, v2
	v_cvt_f32_u32_e32 v2, s0
	s_sub_i32 s9, 0, s0
	s_abs_i32 s5, s10
	s_ashr_i32 s4, s10, 31
	v_rcp_iflag_f32_e32 v2, v2
	v_add_u32_e32 v3, 0xa00, v34
	v_ashrrev_i32_e32 v43, 6, v3
	v_add_u32_e32 v3, 0xc00, v34
	v_mul_f32_e32 v2, 0x4f7ffffe, v2
	v_cvt_u32_f32_e32 v2, v2
	v_lshlrev_b32_e32 v1, 2, v34
	v_ashrrev_i32_e32 v44, 6, v3
	v_add_u32_e32 v3, 0xe00, v34
	v_readfirstlane_b32 s11, v2
	s_mul_i32 s9, s9, s11
	s_mul_hi_u32 s9, s11, s9
	s_add_i32 s11, s11, s9
	s_mul_hi_u32 s9, s5, s11
	s_mul_i32 s11, s9, s0
	s_sub_i32 s5, s5, s11
	s_add_i32 s11, s9, 1
	s_sub_i32 s12, s5, s0
	s_cmp_ge_u32 s5, s0
	s_cselect_b32 s9, s11, s9
	s_cselect_b32 s5, s12, s5
	s_add_i32 s11, s9, 1
	s_cmp_ge_u32 s5, s0
	s_cselect_b32 s5, s11, s9
	s_xor_b32 s5, s5, s4
	s_sub_i32 s9, s5, s4
	s_mul_i32 s0, s9, s0
	s_sub_i32 s0, s10, s0
	s_lshl_b32 s4, s0, 8
	s_ashr_i32 s5, s4, 31
	s_lshl_b64 s[10:11], s[4:5], 2
	s_add_u32 s6, s6, s10
	v_and_b32_e32 v38, 0xfc, v1
	v_ashrrev_i32_e32 v45, 6, v3
	s_addc_u32 s7, s7, s11
	s_lshl_b32 s14, s9, 6
	v_mov_b32_e32 v37, 0
	v_lshlrev_b32_e32 v36, 2, v38
	v_add_u32_e32 v4, s14, v45
	v_lshl_add_u64 v[2:3], s[6:7], 0, v[36:37]
	s_waitcnt vmcnt(10)
	v_ashrrev_i32_e32 v7, 31, v4
	v_mad_u64_u32 v[4:5], s[6:7], v4, s8, 0
	v_mov_b32_e32 v6, v5
	v_mad_u64_u32 v[6:7], s[6:7], v7, s8, v[6:7]
	v_mov_b32_e32 v5, v6
	v_add_u32_e32 v6, s14, v44
	v_ashrrev_i32_e32 v9, 31, v6
	v_mad_u64_u32 v[6:7], s[6:7], v6, s8, 0
	v_mov_b32_e32 v8, v7
	v_mad_u64_u32 v[8:9], s[6:7], v9, s8, v[8:9]
	v_lshl_add_u64 v[4:5], v[4:5], 2, v[2:3]
	v_mov_b32_e32 v7, v8
	v_lshl_add_u64 v[6:7], v[6:7], 2, v[2:3]
	global_load_dwordx4 v[30:33], v[4:5], off nt
	global_load_dwordx4 v[26:29], v[6:7], off nt
	v_add_u32_e32 v4, s14, v43
	v_ashrrev_i32_e32 v7, 31, v4
	v_mad_u64_u32 v[4:5], s[6:7], v4, s8, 0
	v_mov_b32_e32 v6, v5
	v_mad_u64_u32 v[6:7], s[6:7], v7, s8, v[6:7]
	v_mov_b32_e32 v5, v6
	v_add_u32_e32 v6, s14, v42
	v_ashrrev_i32_e32 v9, 31, v6
	v_mad_u64_u32 v[6:7], s[6:7], v6, s8, 0
	v_mov_b32_e32 v8, v7
	v_add_u32_e32 v55, 0x600, v34
	v_mad_u64_u32 v[8:9], s[6:7], v9, s8, v[8:9]
	v_ashrrev_i32_e32 v41, 6, v55
	v_lshl_add_u64 v[4:5], v[4:5], 2, v[2:3]
	v_mov_b32_e32 v7, v8
	v_lshl_add_u64 v[6:7], v[6:7], 2, v[2:3]
	global_load_dwordx4 v[22:25], v[4:5], off nt
	global_load_dwordx4 v[18:21], v[6:7], off nt
	v_add_u32_e32 v4, s14, v41
	v_ashrrev_i32_e32 v7, 31, v4
	v_mad_u64_u32 v[4:5], s[6:7], v4, s8, 0
	v_add_u32_e32 v52, 0x400, v34
	v_mov_b32_e32 v6, v5
	v_ashrrev_i32_e32 v40, 6, v52
	v_mad_u64_u32 v[6:7], s[6:7], v7, s8, v[6:7]
	v_mov_b32_e32 v5, v6
	v_add_u32_e32 v6, s14, v40
	v_ashrrev_i32_e32 v9, 31, v6
	v_mad_u64_u32 v[6:7], s[6:7], v6, s8, 0
	v_mov_b32_e32 v8, v7
	v_add_u32_e32 v35, 0x200, v34
	v_mad_u64_u32 v[8:9], s[6:7], v9, s8, v[8:9]
	v_ashrrev_i32_e32 v39, 6, v35
	v_lshl_add_u64 v[4:5], v[4:5], 2, v[2:3]
	v_mov_b32_e32 v7, v8
	v_lshl_add_u64 v[6:7], v[6:7], 2, v[2:3]
	global_load_dwordx4 v[14:17], v[4:5], off nt
	global_load_dwordx4 v[10:13], v[6:7], off nt
	v_add_u32_e32 v4, s14, v39
	v_ashrrev_i32_e32 v7, 31, v4
	v_mad_u64_u32 v[4:5], s[6:7], v4, s8, 0
	v_mov_b32_e32 v6, v5
	v_ashrrev_i32_e32 v1, 6, v34
	v_mad_u64_u32 v[6:7], s[6:7], v7, s8, v[6:7]
	v_mov_b32_e32 v5, v6
	v_add_u32_e32 v6, s14, v1
	v_ashrrev_i32_e32 v9, 31, v6
	v_mad_u64_u32 v[6:7], s[6:7], v6, s8, 0
	v_mov_b32_e32 v8, v7
	v_mad_u64_u32 v[8:9], s[6:7], v9, s8, v[8:9]
	v_mov_b32_e32 v7, v8
	v_lshl_add_u64 v[4:5], v[4:5], 2, v[2:3]
	v_lshl_add_u64 v[2:3], v[6:7], 2, v[2:3]
	global_load_dwordx4 v[6:9], v[4:5], off nt
	s_nop 0
	global_load_dwordx4 v[2:5], v[2:3], off nt
	v_lshlrev_b32_e32 v46, 3, v34
	v_and_b32_e32 v66, 56, v46
	s_movk_i32 s0, 0x404
	v_readlane_b32 s12, v251, 60
	v_mad_u32_u24 v56, v66, s0, 0
	v_mul_lo_u32 v58, v1, s0
	v_mul_lo_u32 v59, v39, s0
	v_mul_lo_u32 v60, v40, s0
	v_mul_lo_u32 v61, v41, s0
	v_mul_lo_u32 v62, v42, s0
	v_mul_lo_u32 v63, v43, s0
	v_mul_lo_u32 v64, v44, s0
	v_mul_lo_u32 v65, v45, s0
	v_readlane_b32 s13, v251, 61
	s_add_u32 s0, s12, 0x1e940000
	s_addc_u32 s5, s13, 0
	s_add_u32 s8, s12, 0x16940000
	s_addc_u32 s9, s13, 0
	s_add_u32 s10, s12, 0x16140000
	s_addc_u32 s11, s13, 0
	s_add_u32 s27, s12, 0x15540000
	s_addc_u32 s28, s13, 0
	v_add_u32_e32 v36, 0, v36
	v_ashrrev_i32_e32 v46, 3, v34
	v_ashrrev_i32_e32 v49, 3, v35
	v_ashrrev_i32_e32 v52, 3, v52
	v_ashrrev_i32_e32 v55, 3, v55
	s_add_u32 s12, s12, 0x11f40000
	s_mov_b32 s7, 0
	v_lshl_add_u32 v47, v46, 2, v56
	v_and_b32_e32 v48, 15, v46
	v_lshl_add_u32 v50, v49, 2, v56
	v_and_b32_e32 v51, 15, v49
	v_lshl_add_u32 v53, v52, 2, v56
	v_and_b32_e32 v54, 15, v52
	v_lshl_add_u32 v56, v55, 2, v56
	v_and_b32_e32 v57, 15, v55
	s_addc_u32 s13, s13, 0
	s_add_i32 s29, s16, 0xfffffce1
	s_mov_b32 s30, 25
	v_add_u32_e32 v58, v36, v58
	v_add_u32_e32 v59, v36, v59
	v_add_u32_e32 v60, v36, v60
	v_add_u32_e32 v61, v36, v61
	v_add_u32_e32 v62, v36, v62
	v_add_u32_e32 v63, v36, v63
	v_add_u32_e32 v64, v36, v64
	v_add_u32_e32 v65, v36, v65
	v_lshlrev_b32_e32 v36, 2, v38
	v_lshlrev_b32_e32 v34, 1, v66
	s_movk_i32 s31, 0x7fff
	v_mov_b32_e32 v38, 1
	s_mov_b32 s24, s15
	s_mov_b32 s25, s26
	s_mov_b64 s[18:19], s[2:3]
	s_branch .LBB0_1995

.LBB0_1993:
	s_lshr_b32 s20, s36, 8
	v_cvt_f32_u32_e32 v2, s20
	s_sub_i32 s34, 0, s20
	s_abs_i32 s21, s37
	s_ashr_i32 s6, s37, 31
	v_rcp_iflag_f32_e32 v2, v2
	s_nop 0
	v_mul_f32_e32 v2, 0x4f7ffffe, v2
	v_cvt_u32_f32_e32 v2, v2
	s_nop 0
	v_readfirstlane_b32 s38, v2
	s_mul_i32 s34, s34, s38
	s_mul_hi_u32 s34, s38, s34
	s_add_i32 s38, s38, s34
	s_mul_hi_u32 s34, s21, s38
	s_mul_i32 s38, s34, s20
	s_sub_i32 s21, s21, s38
	s_add_i32 s39, s34, 1
	s_sub_i32 s38, s21, s20
	s_cmp_ge_u32 s21, s20
	s_cselect_b32 s34, s39, s34
	s_cselect_b32 s21, s38, s21
	s_add_i32 s38, s34, 1
	s_cmp_ge_u32 s21, s20
	s_cselect_b32 s21, s38, s34
	s_xor_b32 s21, s21, s6
	s_sub_i32 s21, s21, s6
	s_lshl_b32 s6, s21, 6
	s_mul_i32 s21, s21, s20
	s_sub_i32 s20, s37, s21
	s_lshl_b32 s20, s20, 8
	s_ashr_i32 s21, s20, 31
	s_lshl_b64 s[38:39], s[20:21], 2
	s_add_u32 s22, s22, s38
	v_add_u32_e32 v2, s6, v1
	s_addc_u32 s23, s23, s39
	v_add_u32_e32 v10, s6, v40
	v_add_u32_e32 v18, s6, v42
	v_add_u32_e32 v28, s6, v44
	v_ashrrev_i32_e32 v5, 31, v2
	v_lshl_add_u64 v[26:27], s[22:23], 0, v[36:37]
	v_mad_u64_u32 v[2:3], s[22:23], v2, s36, 0
	v_ashrrev_i32_e32 v13, 31, v10
	v_mad_u64_u32 v[10:11], s[22:23], v10, s36, 0
	v_ashrrev_i32_e32 v21, 31, v18
	v_mad_u64_u32 v[18:19], s[22:23], v18, s36, 0
	v_ashrrev_i32_e32 v31, 31, v28
	v_mad_u64_u32 v[28:29], s[22:23], v28, s36, 0
	v_mov_b32_e32 v4, v3
	v_mov_b32_e32 v12, v11
	v_mov_b32_e32 v20, v19
	v_mov_b32_e32 v30, v29
	v_mad_u64_u32 v[4:5], s[22:23], v5, s36, v[4:5]
	v_mad_u64_u32 v[12:13], s[22:23], v13, s36, v[12:13]
	v_mad_u64_u32 v[20:21], s[22:23], v21, s36, v[20:21]
	v_mad_u64_u32 v[30:31], s[22:23], v31, s36, v[30:31]
	v_mov_b32_e32 v3, v4
	v_add_u32_e32 v4, s6, v39
	v_mov_b32_e32 v11, v12
	v_add_u32_e32 v12, s6, v41
	v_mov_b32_e32 v19, v20
	v_add_u32_e32 v20, s6, v43
	v_mov_b32_e32 v29, v30
	v_add_u32_e32 v30, s6, v45
	v_ashrrev_i32_e32 v7, 31, v4
	v_mad_u64_u32 v[4:5], s[22:23], v4, s36, 0
	v_ashrrev_i32_e32 v15, 31, v12
	v_mad_u64_u32 v[12:13], s[22:23], v12, s36, 0
	v_ashrrev_i32_e32 v23, 31, v20
	v_mad_u64_u32 v[20:21], s[22:23], v20, s36, 0
	v_ashrrev_i32_e32 v33, 31, v30
	v_mad_u64_u32 v[30:31], s[22:23], v30, s36, 0
	v_mov_b32_e32 v6, v5
	v_mov_b32_e32 v14, v13
	v_mov_b32_e32 v22, v21
	v_mov_b32_e32 v32, v31
	v_mad_u64_u32 v[6:7], s[22:23], v7, s36, v[6:7]
	v_mad_u64_u32 v[14:15], s[22:23], v15, s36, v[14:15]
	v_mad_u64_u32 v[22:23], s[22:23], v23, s36, v[22:23]
	v_mad_u64_u32 v[32:33], s[22:23], v33, s36, v[32:33]
	v_mov_b32_e32 v5, v6
	v_mov_b32_e32 v13, v14
	v_mov_b32_e32 v21, v22
	v_mov_b32_e32 v31, v32
	v_lshl_add_u64 v[2:3], v[2:3], 2, v[26:27]
	v_lshl_add_u64 v[6:7], v[4:5], 2, v[26:27]
	v_lshl_add_u64 v[10:11], v[10:11], 2, v[26:27]
	v_lshl_add_u64 v[14:15], v[12:13], 2, v[26:27]
	v_lshl_add_u64 v[18:19], v[18:19], 2, v[26:27]
	v_lshl_add_u64 v[22:23], v[20:21], 2, v[26:27]
	v_lshl_add_u64 v[28:29], v[28:29], 2, v[26:27]
	v_lshl_add_u64 v[30:31], v[30:31], 2, v[26:27]
	global_load_dwordx4 v[2:5], v[2:3], off nt
	s_nop 0
	global_load_dwordx4 v[6:9], v[6:7], off nt
	s_nop 0
	global_load_dwordx4 v[10:13], v[10:11], off nt
	s_nop 0
	global_load_dwordx4 v[14:17], v[14:15], off nt
	s_nop 0
	global_load_dwordx4 v[18:21], v[18:19], off nt
	s_nop 0
	global_load_dwordx4 v[22:25], v[22:23], off nt
	s_nop 0
	global_load_dwordx4 v[26:29], v[28:29], off nt
	s_nop 0
	global_load_dwordx4 v[30:33], v[30:31], off nt
.LBB0_1994:
	s_add_i32 s30, s30, -1
	s_cmp_eq_u32 s15, 0
	v_add_u32_e32 v66, s4, v46
	v_lshlrev_b32_e32 v35, 1, v66
	s_cselect_b64 vcc, -1, 0
	s_ashr_i32 s15, s14, 31
	v_and_b32_e32 v35, 0xffffffe0, v35
	s_lshl_b64 s[14:15], s[14:15], 1
	v_add3_u32 v67, s1, v48, v35
	s_add_u32 s2, s2, s14
	s_addc_u32 s3, s3, s15
	v_mov_b32_e32 v35, v37
	v_cndmask_b32_e32 v66, v67, v66, vcc
	v_lshl_add_u64 v[70:71], s[2:3], 0, v[34:35]
	v_ashrrev_i32_e32 v69, 31, v66
	v_mad_u64_u32 v[66:67], s[2:3], v66, s26, 0
	v_mov_b32_e32 v68, v67
	ds_read_b32 v35, v47
	ds_read_b32 v74, v47 offset:1028
	ds_read_b32 v75, v47 offset:2056
	ds_read_b32 v76, v47 offset:3084
	ds_read_b32 v77, v47 offset:4112
	ds_read_b32 v78, v47 offset:5140
	ds_read_b32 v79, v47 offset:6168
	ds_read_b32 v80, v47 offset:7196
	v_mad_u64_u32 v[68:69], s[2:3], v69, s26, v[68:69]
	v_mov_b32_e32 v67, v68
	v_lshl_add_u64 v[72:73], v[66:67], 1, v[70:71]
	s_waitcnt lgkmcnt(7)
	v_and_b32_sdwa v67, v35, v38 dst_sel:DWORD dst_unused:UNUSED_PAD src0_sel:WORD_1 src1_sel:DWORD
	v_add3_u32 v35, v35, v67, s31
	s_waitcnt lgkmcnt(4)
	v_and_b32_sdwa v67, v76, v38 dst_sel:DWORD dst_unused:UNUSED_PAD src0_sel:WORD_1 src1_sel:DWORD
	v_and_b32_sdwa v68, v74, v38 dst_sel:DWORD dst_unused:UNUSED_PAD src0_sel:WORD_1 src1_sel:DWORD
	v_and_b32_sdwa v66, v75, v38 dst_sel:DWORD dst_unused:UNUSED_PAD src0_sel:WORD_1 src1_sel:DWORD
	v_add3_u32 v67, v76, v67, s31
	v_add3_u32 v68, v74, v68, s31
	v_add3_u32 v66, v75, v66, s31
	v_and_b32_e32 v67, 0xffff0000, v67
	v_and_b32_e32 v68, 0xffff0000, v68
	s_waitcnt lgkmcnt(0)
	v_and_b32_sdwa v69, v80, v38 dst_sel:DWORD dst_unused:UNUSED_PAD src0_sel:WORD_1 src1_sel:DWORD
	v_and_b32_sdwa v74, v78, v38 dst_sel:DWORD dst_unused:UNUSED_PAD src0_sel:WORD_1 src1_sel:DWORD
	v_or_b32_sdwa v67, v67, v66 dst_sel:DWORD dst_unused:UNUSED_PAD src0_sel:DWORD src1_sel:WORD_1
	v_or_b32_sdwa v66, v68, v35 dst_sel:DWORD dst_unused:UNUSED_PAD src0_sel:DWORD src1_sel:WORD_1
	v_and_b32_sdwa v35, v79, v38 dst_sel:DWORD dst_unused:UNUSED_PAD src0_sel:WORD_1 src1_sel:DWORD
	v_and_b32_sdwa v68, v77, v38 dst_sel:DWORD dst_unused:UNUSED_PAD src0_sel:WORD_1 src1_sel:DWORD
	v_add3_u32 v69, v80, v69, s31
	v_add3_u32 v74, v78, v74, s31
	v_add3_u32 v68, v77, v68, s31
	v_add3_u32 v35, v79, v35, s31
	v_and_b32_e32 v69, 0xffff0000, v69
	v_and_b32_e32 v74, 0xffff0000, v74
	v_or_b32_sdwa v69, v69, v35 dst_sel:DWORD dst_unused:UNUSED_PAD src0_sel:DWORD src1_sel:WORD_1
	v_or_b32_sdwa v68, v74, v68 dst_sel:DWORD dst_unused:UNUSED_PAD src0_sel:DWORD src1_sel:WORD_1
	global_store_dwordx4 v[72:73], v[66:69], off nt
	ds_read_b32 v35, v50
	ds_read_b32 v74, v50 offset:1028
	ds_read_b32 v75, v50 offset:2056
	ds_read_b32 v76, v50 offset:3084
	ds_read_b32 v77, v50 offset:4112
	ds_read_b32 v78, v50 offset:5140
	ds_read_b32 v79, v50 offset:6168
	ds_read_b32 v80, v50 offset:7196
	v_add_u32_e32 v66, s4, v49
	v_lshlrev_b32_e32 v67, 1, v66
	v_and_b32_e32 v67, 0xffffffe0, v67
	v_add3_u32 v67, s1, v51, v67
	v_cndmask_b32_e32 v66, v67, v66, vcc
	v_ashrrev_i32_e32 v69, 31, v66
	v_mad_u64_u32 v[66:67], s[2:3], v66, s26, 0
	v_mov_b32_e32 v68, v67
	v_mad_u64_u32 v[68:69], s[2:3], v69, s26, v[68:69]
	v_mov_b32_e32 v67, v68
	v_lshl_add_u64 v[72:73], v[66:67], 1, v[70:71]
	s_waitcnt lgkmcnt(7)
	v_and_b32_sdwa v67, v35, v38 dst_sel:DWORD dst_unused:UNUSED_PAD src0_sel:WORD_1 src1_sel:DWORD
	v_add3_u32 v35, v35, v67, s31
	s_waitcnt lgkmcnt(4)
	v_and_b32_sdwa v67, v76, v38 dst_sel:DWORD dst_unused:UNUSED_PAD src0_sel:WORD_1 src1_sel:DWORD
	v_and_b32_sdwa v68, v74, v38 dst_sel:DWORD dst_unused:UNUSED_PAD src0_sel:WORD_1 src1_sel:DWORD
	v_and_b32_sdwa v66, v75, v38 dst_sel:DWORD dst_unused:UNUSED_PAD src0_sel:WORD_1 src1_sel:DWORD
	v_add3_u32 v67, v76, v67, s31
	v_add3_u32 v68, v74, v68, s31
	v_add3_u32 v66, v75, v66, s31
	v_and_b32_e32 v67, 0xffff0000, v67
	v_and_b32_e32 v68, 0xffff0000, v68
	s_waitcnt lgkmcnt(0)
	v_and_b32_sdwa v69, v80, v38 dst_sel:DWORD dst_unused:UNUSED_PAD src0_sel:WORD_1 src1_sel:DWORD
	v_and_b32_sdwa v74, v78, v38 dst_sel:DWORD dst_unused:UNUSED_PAD src0_sel:WORD_1 src1_sel:DWORD
	v_or_b32_sdwa v67, v67, v66 dst_sel:DWORD dst_unused:UNUSED_PAD src0_sel:DWORD src1_sel:WORD_1
	v_or_b32_sdwa v66, v68, v35 dst_sel:DWORD dst_unused:UNUSED_PAD src0_sel:DWORD src1_sel:WORD_1
	v_and_b32_sdwa v35, v79, v38 dst_sel:DWORD dst_unused:UNUSED_PAD src0_sel:WORD_1 src1_sel:DWORD
	v_and_b32_sdwa v68, v77, v38 dst_sel:DWORD dst_unused:UNUSED_PAD src0_sel:WORD_1 src1_sel:DWORD
	v_add3_u32 v69, v80, v69, s31
	v_add3_u32 v74, v78, v74, s31
	v_add3_u32 v68, v77, v68, s31
	v_add3_u32 v35, v79, v35, s31
	v_and_b32_e32 v69, 0xffff0000, v69
	v_and_b32_e32 v74, 0xffff0000, v74
	v_or_b32_sdwa v69, v69, v35 dst_sel:DWORD dst_unused:UNUSED_PAD src0_sel:DWORD src1_sel:WORD_1
	v_or_b32_sdwa v68, v74, v68 dst_sel:DWORD dst_unused:UNUSED_PAD src0_sel:DWORD src1_sel:WORD_1
	global_store_dwordx4 v[72:73], v[66:69], off nt
	ds_read_b32 v35, v53
	ds_read_b32 v74, v53 offset:1028
	ds_read_b32 v75, v53 offset:2056
	ds_read_b32 v76, v53 offset:3084
	ds_read_b32 v77, v53 offset:4112
	ds_read_b32 v78, v53 offset:5140
	ds_read_b32 v79, v53 offset:6168
	ds_read_b32 v80, v53 offset:7196
	v_add_u32_e32 v66, s4, v52
	v_lshlrev_b32_e32 v67, 1, v66
	v_and_b32_e32 v67, 0xffffffe0, v67
	v_add3_u32 v67, s1, v54, v67
	v_cndmask_b32_e32 v66, v67, v66, vcc
	v_ashrrev_i32_e32 v69, 31, v66
	v_mad_u64_u32 v[66:67], s[2:3], v66, s26, 0
	v_mov_b32_e32 v68, v67
	v_mad_u64_u32 v[68:69], s[2:3], v69, s26, v[68:69]
	v_mov_b32_e32 v67, v68
	v_lshl_add_u64 v[72:73], v[66:67], 1, v[70:71]
	s_waitcnt lgkmcnt(7)
	v_and_b32_sdwa v67, v35, v38 dst_sel:DWORD dst_unused:UNUSED_PAD src0_sel:WORD_1 src1_sel:DWORD
	v_add3_u32 v35, v35, v67, s31
	s_waitcnt lgkmcnt(4)
	v_and_b32_sdwa v67, v76, v38 dst_sel:DWORD dst_unused:UNUSED_PAD src0_sel:WORD_1 src1_sel:DWORD
	v_and_b32_sdwa v68, v74, v38 dst_sel:DWORD dst_unused:UNUSED_PAD src0_sel:WORD_1 src1_sel:DWORD
	v_and_b32_sdwa v66, v75, v38 dst_sel:DWORD dst_unused:UNUSED_PAD src0_sel:WORD_1 src1_sel:DWORD
	v_add3_u32 v67, v76, v67, s31
	v_add3_u32 v68, v74, v68, s31
	v_add3_u32 v66, v75, v66, s31
	v_and_b32_e32 v67, 0xffff0000, v67
	v_and_b32_e32 v68, 0xffff0000, v68
	s_waitcnt lgkmcnt(0)
	v_and_b32_sdwa v69, v80, v38 dst_sel:DWORD dst_unused:UNUSED_PAD src0_sel:WORD_1 src1_sel:DWORD
	v_and_b32_sdwa v74, v78, v38 dst_sel:DWORD dst_unused:UNUSED_PAD src0_sel:WORD_1 src1_sel:DWORD
	v_or_b32_sdwa v67, v67, v66 dst_sel:DWORD dst_unused:UNUSED_PAD src0_sel:DWORD src1_sel:WORD_1
	v_or_b32_sdwa v66, v68, v35 dst_sel:DWORD dst_unused:UNUSED_PAD src0_sel:DWORD src1_sel:WORD_1
	v_and_b32_sdwa v35, v79, v38 dst_sel:DWORD dst_unused:UNUSED_PAD src0_sel:WORD_1 src1_sel:DWORD
	v_and_b32_sdwa v68, v77, v38 dst_sel:DWORD dst_unused:UNUSED_PAD src0_sel:WORD_1 src1_sel:DWORD
	v_add3_u32 v69, v80, v69, s31
	v_add3_u32 v74, v78, v74, s31
	v_add3_u32 v68, v77, v68, s31
	v_add3_u32 v35, v79, v35, s31
	v_and_b32_e32 v69, 0xffff0000, v69
	v_and_b32_e32 v74, 0xffff0000, v74
	v_or_b32_sdwa v69, v69, v35 dst_sel:DWORD dst_unused:UNUSED_PAD src0_sel:DWORD src1_sel:WORD_1
	v_or_b32_sdwa v68, v74, v68 dst_sel:DWORD dst_unused:UNUSED_PAD src0_sel:DWORD src1_sel:WORD_1
	global_store_dwordx4 v[72:73], v[66:69], off nt
	ds_read_b32 v35, v56
	ds_read_b32 v72, v56 offset:1028
	ds_read_b32 v73, v56 offset:2056
	ds_read_b32 v74, v56 offset:3084
	ds_read_b32 v75, v56 offset:4112
	ds_read_b32 v76, v56 offset:5140
	ds_read_b32 v77, v56 offset:6168
	ds_read_b32 v78, v56 offset:7196
	v_add_u32_e32 v66, s4, v55
	v_lshlrev_b32_e32 v67, 1, v66
	v_and_b32_e32 v67, 0xffffffe0, v67
	v_add3_u32 v67, s1, v57, v67
	v_cndmask_b32_e32 v66, v67, v66, vcc
	v_ashrrev_i32_e32 v69, 31, v66
	v_mad_u64_u32 v[66:67], s[2:3], v66, s26, 0
	v_mov_b32_e32 v68, v67
	v_mad_u64_u32 v[68:69], s[2:3], v69, s26, v[68:69]
	v_mov_b32_e32 v67, v68
	v_lshl_add_u64 v[70:71], v[66:67], 1, v[70:71]
	s_waitcnt lgkmcnt(7)
	v_and_b32_sdwa v67, v35, v38 dst_sel:DWORD dst_unused:UNUSED_PAD src0_sel:WORD_1 src1_sel:DWORD
	v_add3_u32 v35, v35, v67, s31
	s_waitcnt lgkmcnt(4)
	v_and_b32_sdwa v67, v74, v38 dst_sel:DWORD dst_unused:UNUSED_PAD src0_sel:WORD_1 src1_sel:DWORD
	v_and_b32_sdwa v68, v72, v38 dst_sel:DWORD dst_unused:UNUSED_PAD src0_sel:WORD_1 src1_sel:DWORD
	v_and_b32_sdwa v66, v73, v38 dst_sel:DWORD dst_unused:UNUSED_PAD src0_sel:WORD_1 src1_sel:DWORD
	v_add3_u32 v67, v74, v67, s31
	v_add3_u32 v68, v72, v68, s31
	v_add3_u32 v66, v73, v66, s31
	v_and_b32_e32 v67, 0xffff0000, v67
	v_and_b32_e32 v68, 0xffff0000, v68
	s_waitcnt lgkmcnt(0)
	v_and_b32_sdwa v69, v78, v38 dst_sel:DWORD dst_unused:UNUSED_PAD src0_sel:WORD_1 src1_sel:DWORD
	v_and_b32_sdwa v72, v76, v38 dst_sel:DWORD dst_unused:UNUSED_PAD src0_sel:WORD_1 src1_sel:DWORD
	v_or_b32_sdwa v67, v67, v66 dst_sel:DWORD dst_unused:UNUSED_PAD src0_sel:DWORD src1_sel:WORD_1
	v_or_b32_sdwa v66, v68, v35 dst_sel:DWORD dst_unused:UNUSED_PAD src0_sel:DWORD src1_sel:WORD_1
	v_and_b32_sdwa v35, v77, v38 dst_sel:DWORD dst_unused:UNUSED_PAD src0_sel:WORD_1 src1_sel:DWORD
	v_and_b32_sdwa v68, v75, v38 dst_sel:DWORD dst_unused:UNUSED_PAD src0_sel:WORD_1 src1_sel:DWORD
	v_add3_u32 v69, v78, v69, s31
	v_add3_u32 v72, v76, v72, s31
	v_add3_u32 v68, v75, v68, s31
	v_add3_u32 v35, v77, v35, s31
	v_and_b32_e32 v69, 0xffff0000, v69
	v_and_b32_e32 v72, 0xffff0000, v72
	v_or_b32_sdwa v69, v69, v35 dst_sel:DWORD dst_unused:UNUSED_PAD src0_sel:DWORD src1_sel:WORD_1
	v_or_b32_sdwa v68, v72, v68 dst_sel:DWORD dst_unused:UNUSED_PAD src0_sel:DWORD src1_sel:WORD_1
	s_add_i32 s29, s29, 1
	s_and_b64 vcc, exec, s[16:17]
	s_mov_b32 s34, s33
	s_mov_b32 s1, s35
	s_mov_b32 s15, s24
	s_mov_b32 s4, s20
	s_mov_b32 s14, s6
	s_mov_b32 s26, s25
	s_mov_b64 s[2:3], s[18:19]
	global_store_dwordx4 v[70:71], v[66:69], off nt
	s_barrier
	s_cbranch_vccnz .LBB0_2013

.LBB0_2313:
	s_waitcnt vmcnt(11)
	v_add_u32_e32 v2, 0x800, v130
	s_lshr_b32 s0, s12, 8
	v_ashrrev_i32_e32 v41, 6, v2
	v_cvt_f32_u32_e32 v2, s0
	s_sub_i32 s14, 0, s0
	s_abs_i32 s9, s13
	s_ashr_i32 s8, s13, 31
	v_rcp_iflag_f32_e32 v2, v2
	v_add_u32_e32 v3, 0xa00, v130
	v_ashrrev_i32_e32 v42, 6, v3
	v_add_u32_e32 v3, 0xc00, v130
	v_mul_f32_e32 v2, 0x4f7ffffe, v2
	v_cvt_u32_f32_e32 v2, v2
	v_lshlrev_b32_e32 v1, 2, v130
	v_ashrrev_i32_e32 v43, 6, v3
	v_add_u32_e32 v3, 0xe00, v130
	v_readfirstlane_b32 s15, v2
	s_mul_i32 s14, s14, s15
	s_mul_hi_u32 s14, s15, s14
	s_add_i32 s15, s15, s14
	s_mul_hi_u32 s14, s9, s15
	s_mul_i32 s15, s14, s0
	s_sub_i32 s9, s9, s15
	s_add_i32 s15, s14, 1
	s_sub_i32 s16, s9, s0
	s_cmp_ge_u32 s9, s0
	s_cselect_b32 s14, s15, s14
	s_cselect_b32 s9, s16, s9
	s_add_i32 s15, s14, 1
	s_cmp_ge_u32 s9, s0
	s_cselect_b32 s9, s15, s14
	s_xor_b32 s9, s9, s8
	s_sub_i32 s16, s9, s8
	s_mul_i32 s0, s16, s0
	s_sub_i32 s0, s13, s0
	s_lshl_b32 s8, s0, 8
	s_ashr_i32 s9, s8, 31
	s_lshl_b64 s[14:15], s[8:9], 2
	s_add_u32 s10, s10, s14
	v_and_b32_e32 v36, 0xfc, v1
	v_ashrrev_i32_e32 v44, 6, v3
	s_addc_u32 s11, s11, s15
	s_lshl_b32 s20, s16, 6
	v_mov_b32_e32 v35, 0
	v_lshlrev_b32_e32 v34, 2, v36
	v_add_u32_e32 v4, s20, v44
	v_lshl_add_u64 v[2:3], s[10:11], 0, v[34:35]
	s_waitcnt vmcnt(10)
	v_ashrrev_i32_e32 v7, 31, v4
	v_mad_u64_u32 v[4:5], s[10:11], v4, s12, 0
	v_mov_b32_e32 v6, v5
	v_mad_u64_u32 v[6:7], s[10:11], v7, s12, v[6:7]
	v_mov_b32_e32 v5, v6
	v_add_u32_e32 v6, s20, v43
	v_ashrrev_i32_e32 v9, 31, v6
	v_mad_u64_u32 v[6:7], s[10:11], v6, s12, 0
	v_mov_b32_e32 v8, v7
	v_mad_u64_u32 v[8:9], s[10:11], v9, s12, v[8:9]
	v_lshl_add_u64 v[4:5], v[4:5], 2, v[2:3]
	v_mov_b32_e32 v7, v8
	v_lshl_add_u64 v[6:7], v[6:7], 2, v[2:3]
	global_load_dwordx4 v[30:33], v[4:5], off nt
	global_load_dwordx4 v[26:29], v[6:7], off nt
	v_add_u32_e32 v4, s20, v42
	v_ashrrev_i32_e32 v7, 31, v4
	v_mad_u64_u32 v[4:5], s[10:11], v4, s12, 0
	v_mov_b32_e32 v6, v5
	v_mad_u64_u32 v[6:7], s[10:11], v7, s12, v[6:7]
	v_mov_b32_e32 v5, v6
	v_add_u32_e32 v6, s20, v41
	v_ashrrev_i32_e32 v9, 31, v6
	v_mad_u64_u32 v[6:7], s[10:11], v6, s12, 0
	v_mov_b32_e32 v8, v7
	v_add_u32_e32 v54, 0x600, v130
	v_mad_u64_u32 v[8:9], s[10:11], v9, s12, v[8:9]
	v_ashrrev_i32_e32 v40, 6, v54
	v_lshl_add_u64 v[4:5], v[4:5], 2, v[2:3]
	v_mov_b32_e32 v7, v8
	v_lshl_add_u64 v[6:7], v[6:7], 2, v[2:3]
	global_load_dwordx4 v[22:25], v[4:5], off nt
	global_load_dwordx4 v[18:21], v[6:7], off nt
	v_add_u32_e32 v4, s20, v40
	v_ashrrev_i32_e32 v7, 31, v4
	v_mad_u64_u32 v[4:5], s[10:11], v4, s12, 0
	v_add_u32_e32 v51, 0x400, v130
	v_mov_b32_e32 v6, v5
	v_ashrrev_i32_e32 v39, 6, v51
	v_mad_u64_u32 v[6:7], s[10:11], v7, s12, v[6:7]
	v_mov_b32_e32 v5, v6
	v_add_u32_e32 v6, s20, v39
	v_ashrrev_i32_e32 v9, 31, v6
	v_mad_u64_u32 v[6:7], s[10:11], v6, s12, 0
	v_mov_b32_e32 v8, v7
	v_add_u32_e32 v37, 0x200, v130
	v_mad_u64_u32 v[8:9], s[10:11], v9, s12, v[8:9]
	v_ashrrev_i32_e32 v38, 6, v37
	v_lshl_add_u64 v[4:5], v[4:5], 2, v[2:3]
	v_mov_b32_e32 v7, v8
	v_lshl_add_u64 v[6:7], v[6:7], 2, v[2:3]
	global_load_dwordx4 v[14:17], v[4:5], off nt
	global_load_dwordx4 v[10:13], v[6:7], off nt
	v_add_u32_e32 v4, s20, v38
	v_ashrrev_i32_e32 v7, 31, v4
	v_mad_u64_u32 v[4:5], s[10:11], v4, s12, 0
	v_mov_b32_e32 v6, v5
	v_ashrrev_i32_e32 v1, 6, v130
	v_mad_u64_u32 v[6:7], s[10:11], v7, s12, v[6:7]
	v_mov_b32_e32 v5, v6
	v_add_u32_e32 v6, s20, v1
	v_ashrrev_i32_e32 v9, 31, v6
	v_mad_u64_u32 v[6:7], s[10:11], v6, s12, 0
	v_mov_b32_e32 v8, v7
	v_mad_u64_u32 v[8:9], s[10:11], v9, s12, v[8:9]
	v_mov_b32_e32 v7, v8
	v_lshl_add_u64 v[4:5], v[4:5], 2, v[2:3]
	v_lshl_add_u64 v[2:3], v[6:7], 2, v[2:3]
	global_load_dwordx4 v[6:9], v[4:5], off nt
	s_nop 0
	global_load_dwordx4 v[2:5], v[2:3], off nt
	v_lshlrev_b32_e32 v45, 3, v130
	v_and_b32_e32 v66, 56, v45
	s_movk_i32 s0, 0x404
	v_mad_u32_u24 v55, v66, s0, 0
	v_mul_lo_u32 v57, v1, s0
	v_mul_lo_u32 v58, v38, s0
	v_mul_lo_u32 v59, v39, s0
	v_mul_lo_u32 v60, v40, s0
	v_mul_lo_u32 v61, v41, s0
	v_mul_lo_u32 v62, v42, s0
	v_mul_lo_u32 v63, v43, s0
	v_mul_lo_u32 v64, v44, s0
	s_add_u32 s0, s6, 0x1e940000
	s_addc_u32 s9, s7, 0
	s_add_u32 s12, s6, 0x16940000
	s_addc_u32 s13, s7, 0
	s_add_u32 s14, s78, 0x1000000
	s_addc_u32 s15, s79, 0
	s_add_u32 s16, s6, 0x16140000
	s_addc_u32 s17, s7, 0
	v_readlane_b32 s56, v250, 7
	s_add_u32 s36, s6, 0x15540000
	v_readlane_b32 s70, v250, 21
	v_readlane_b32 s71, v250, 22
	s_addc_u32 s37, s7, 0
	s_mov_b64 s[18:19], s[70:71]
	s_add_u32 s18, s18, 0x6c00000
	s_addc_u32 s19, s19, 0
	s_add_u32 s6, s6, 0x11f40000
	v_add_u32_e32 v34, 0, v34
	v_ashrrev_i32_e32 v45, 3, v130
	v_ashrrev_i32_e32 v48, 3, v37
	v_ashrrev_i32_e32 v51, 3, v51
	v_ashrrev_i32_e32 v54, 3, v54
	s_addc_u32 s7, s7, 0
	s_add_i32 s10, s33, s40
	s_mov_b32 s11, 0
	v_lshl_add_u32 v46, v45, 2, v55
	v_and_b32_e32 v47, 15, v45
	v_lshl_add_u32 v49, v48, 2, v55
	v_and_b32_e32 v50, 15, v48
	v_lshl_add_u32 v52, v51, 2, v55
	v_and_b32_e32 v53, 15, v51
	v_lshl_add_u32 v55, v54, 2, v55
	v_and_b32_e32 v56, 15, v54
	s_add_i32 s38, s10, 0xfffff5c0
	s_add_i32 s39, s10, 0xfffff6c0
	v_add_u32_e32 v57, v34, v57
	v_add_u32_e32 v58, v34, v58
	v_add_u32_e32 v59, v34, v59
	v_add_u32_e32 v60, v34, v60
	v_add_u32_e32 v61, v34, v61
	v_add_u32_e32 v62, v34, v62
	v_add_u32_e32 v63, v34, v63
	v_add_u32_e32 v64, v34, v64
	v_lshlrev_b32_e32 v34, 2, v36
	v_lshlrev_b32_e32 v36, 1, v66
	s_movk_i32 s41, 0x7fff
	v_mov_b32_e32 v65, 1
	s_mov_b32 s10, s21
	s_mov_b32 s42, s35
	s_mov_b64 s[24:25], s[2:3]
	v_readlane_b32 s57, v250, 8
	v_readlane_b32 s58, v250, 9
	v_readlane_b32 s59, v250, 10
	v_readlane_b32 s60, v250, 11
	v_readlane_b32 s61, v250, 12
	v_readlane_b32 s62, v250, 13
	v_readlane_b32 s63, v250, 14
	v_readlane_b32 s64, v250, 15
	v_readlane_b32 s65, v250, 16
	v_readlane_b32 s66, v250, 17
	v_readlane_b32 s67, v250, 18
	v_readlane_b32 s68, v250, 19
	v_readlane_b32 s69, v250, 20
	s_branch .LBB0_2317

.LBB0_2315:
	s_lshr_b32 s26, s44, 8
	v_cvt_f32_u32_e32 v2, s26
	s_sub_i32 s31, 0, s26
	s_abs_i32 s30, s45
	s_ashr_i32 s27, s45, 31
	v_rcp_iflag_f32_e32 v2, v2
	s_nop 0
	v_mul_f32_e32 v2, 0x4f7ffffe, v2
	v_cvt_u32_f32_e32 v2, v2
	s_nop 0
	v_readfirstlane_b32 s46, v2
	s_mul_i32 s31, s31, s46
	s_mul_hi_u32 s31, s46, s31
	s_add_i32 s46, s46, s31
	s_mul_hi_u32 s31, s30, s46
	s_mul_i32 s46, s31, s26
	s_sub_i32 s30, s30, s46
	s_add_i32 s47, s31, 1
	s_sub_i32 s46, s30, s26
	s_cmp_ge_u32 s30, s26
	s_cselect_b32 s31, s47, s31
	s_cselect_b32 s30, s46, s30
	s_add_i32 s46, s31, 1
	s_cmp_ge_u32 s30, s26
	s_cselect_b32 s30, s46, s31
	s_xor_b32 s30, s30, s27
	s_sub_i32 s27, s30, s27
	s_lshl_b32 s30, s27, 6
	s_mul_i32 s27, s27, s26
	s_sub_i32 s26, s45, s27
	s_lshl_b32 s26, s26, 8
	s_ashr_i32 s27, s26, 31
	s_lshl_b64 s[46:47], s[26:27], 2
	s_add_u32 s28, s28, s46
	v_add_u32_e32 v2, s30, v1
	s_addc_u32 s29, s29, s47
	v_add_u32_e32 v10, s30, v39
	v_add_u32_e32 v18, s30, v41
	v_add_u32_e32 v28, s30, v43
	v_ashrrev_i32_e32 v5, 31, v2
	v_lshl_add_u64 v[26:27], s[28:29], 0, v[34:35]
	v_mad_u64_u32 v[2:3], s[28:29], v2, s44, 0
	v_ashrrev_i32_e32 v13, 31, v10
	v_mad_u64_u32 v[10:11], s[28:29], v10, s44, 0
	v_ashrrev_i32_e32 v21, 31, v18
	v_mad_u64_u32 v[18:19], s[28:29], v18, s44, 0
	v_ashrrev_i32_e32 v31, 31, v28
	v_mad_u64_u32 v[28:29], s[28:29], v28, s44, 0
	v_mov_b32_e32 v4, v3
	v_mov_b32_e32 v12, v11
	v_mov_b32_e32 v20, v19
	v_mov_b32_e32 v30, v29
	v_mad_u64_u32 v[4:5], s[28:29], v5, s44, v[4:5]
	v_mad_u64_u32 v[12:13], s[28:29], v13, s44, v[12:13]
	v_mad_u64_u32 v[20:21], s[28:29], v21, s44, v[20:21]
	v_mad_u64_u32 v[30:31], s[28:29], v31, s44, v[30:31]
	v_mov_b32_e32 v3, v4
	v_add_u32_e32 v4, s30, v38
	v_mov_b32_e32 v11, v12
	v_add_u32_e32 v12, s30, v40
	v_mov_b32_e32 v19, v20
	v_add_u32_e32 v20, s30, v42
	v_mov_b32_e32 v29, v30
	v_add_u32_e32 v30, s30, v44
	v_ashrrev_i32_e32 v7, 31, v4
	v_mad_u64_u32 v[4:5], s[28:29], v4, s44, 0
	v_ashrrev_i32_e32 v15, 31, v12
	v_mad_u64_u32 v[12:13], s[28:29], v12, s44, 0
	v_ashrrev_i32_e32 v23, 31, v20
	v_mad_u64_u32 v[20:21], s[28:29], v20, s44, 0
	v_ashrrev_i32_e32 v33, 31, v30
	v_mad_u64_u32 v[30:31], s[28:29], v30, s44, 0
	v_mov_b32_e32 v6, v5
	v_mov_b32_e32 v14, v13
	v_mov_b32_e32 v22, v21
	v_mov_b32_e32 v32, v31
	v_mad_u64_u32 v[6:7], s[28:29], v7, s44, v[6:7]
	v_mad_u64_u32 v[14:15], s[28:29], v15, s44, v[14:15]
	v_mad_u64_u32 v[22:23], s[28:29], v23, s44, v[22:23]
	v_mad_u64_u32 v[32:33], s[28:29], v33, s44, v[32:33]
	v_mov_b32_e32 v5, v6
	v_mov_b32_e32 v13, v14
	v_mov_b32_e32 v21, v22
	v_mov_b32_e32 v31, v32
	v_lshl_add_u64 v[2:3], v[2:3], 2, v[26:27]
	v_lshl_add_u64 v[6:7], v[4:5], 2, v[26:27]
	v_lshl_add_u64 v[10:11], v[10:11], 2, v[26:27]
	v_lshl_add_u64 v[14:15], v[12:13], 2, v[26:27]
	v_lshl_add_u64 v[18:19], v[18:19], 2, v[26:27]
	v_lshl_add_u64 v[22:23], v[20:21], 2, v[26:27]
	v_lshl_add_u64 v[28:29], v[28:29], 2, v[26:27]
	v_lshl_add_u64 v[30:31], v[30:31], 2, v[26:27]
	global_load_dwordx4 v[2:5], v[2:3], off nt
	s_nop 0
	global_load_dwordx4 v[6:9], v[6:7], off nt
	s_nop 0
	global_load_dwordx4 v[10:13], v[10:11], off nt
	s_nop 0
	global_load_dwordx4 v[14:17], v[14:15], off nt
	s_nop 0
	global_load_dwordx4 v[18:21], v[18:19], off nt
	s_nop 0
	global_load_dwordx4 v[22:25], v[22:23], off nt
	s_nop 0
	global_load_dwordx4 v[26:29], v[28:29], off nt
	s_nop 0
	global_load_dwordx4 v[30:33], v[30:31], off nt
.LBB0_2316:
	s_add_i32 s34, s34, -1
	s_cmp_eq_u32 s21, 0
	v_add_u32_e32 v66, s8, v45
	v_lshlrev_b32_e32 v37, 1, v66
	s_cselect_b64 vcc, -1, 0
	s_ashr_i32 s21, s20, 31
	v_and_b32_e32 v37, 0xffffffe0, v37
	s_lshl_b64 s[20:21], s[20:21], 1
	v_add3_u32 v67, s1, v47, v37
	s_add_u32 s2, s2, s20
	s_addc_u32 s3, s3, s21
	v_mov_b32_e32 v37, v35
	v_cndmask_b32_e32 v66, v67, v66, vcc
	v_lshl_add_u64 v[70:71], s[2:3], 0, v[36:37]
	v_ashrrev_i32_e32 v69, 31, v66
	v_mad_u64_u32 v[66:67], s[2:3], v66, s35, 0
	v_mov_b32_e32 v68, v67
	ds_read_b32 v37, v46
	ds_read_b32 v74, v46 offset:1028
	ds_read_b32 v75, v46 offset:2056
	ds_read_b32 v76, v46 offset:3084
	ds_read_b32 v77, v46 offset:4112
	ds_read_b32 v78, v46 offset:5140
	ds_read_b32 v79, v46 offset:6168
	ds_read_b32 v80, v46 offset:7196
	v_mad_u64_u32 v[68:69], s[2:3], v69, s35, v[68:69]
	v_mov_b32_e32 v67, v68
	v_lshl_add_u64 v[72:73], v[66:67], 1, v[70:71]
	s_waitcnt lgkmcnt(7)
	v_and_b32_sdwa v67, v37, v65 dst_sel:DWORD dst_unused:UNUSED_PAD src0_sel:WORD_1 src1_sel:DWORD
	v_add3_u32 v37, v37, v67, s41
	s_waitcnt lgkmcnt(4)
	v_and_b32_sdwa v67, v76, v65 dst_sel:DWORD dst_unused:UNUSED_PAD src0_sel:WORD_1 src1_sel:DWORD
	v_and_b32_sdwa v68, v74, v65 dst_sel:DWORD dst_unused:UNUSED_PAD src0_sel:WORD_1 src1_sel:DWORD
	v_and_b32_sdwa v66, v75, v65 dst_sel:DWORD dst_unused:UNUSED_PAD src0_sel:WORD_1 src1_sel:DWORD
	v_add3_u32 v67, v76, v67, s41
	v_add3_u32 v68, v74, v68, s41
	v_add3_u32 v66, v75, v66, s41
	v_and_b32_e32 v67, 0xffff0000, v67
	v_and_b32_e32 v68, 0xffff0000, v68
	s_waitcnt lgkmcnt(0)
	v_and_b32_sdwa v69, v80, v65 dst_sel:DWORD dst_unused:UNUSED_PAD src0_sel:WORD_1 src1_sel:DWORD
	v_and_b32_sdwa v74, v78, v65 dst_sel:DWORD dst_unused:UNUSED_PAD src0_sel:WORD_1 src1_sel:DWORD
	v_or_b32_sdwa v67, v67, v66 dst_sel:DWORD dst_unused:UNUSED_PAD src0_sel:DWORD src1_sel:WORD_1
	v_or_b32_sdwa v66, v68, v37 dst_sel:DWORD dst_unused:UNUSED_PAD src0_sel:DWORD src1_sel:WORD_1
	v_and_b32_sdwa v37, v79, v65 dst_sel:DWORD dst_unused:UNUSED_PAD src0_sel:WORD_1 src1_sel:DWORD
	v_and_b32_sdwa v68, v77, v65 dst_sel:DWORD dst_unused:UNUSED_PAD src0_sel:WORD_1 src1_sel:DWORD
	v_add3_u32 v69, v80, v69, s41
	v_add3_u32 v74, v78, v74, s41
	v_add3_u32 v68, v77, v68, s41
	v_add3_u32 v37, v79, v37, s41
	v_and_b32_e32 v69, 0xffff0000, v69
	v_and_b32_e32 v74, 0xffff0000, v74
	v_or_b32_sdwa v69, v69, v37 dst_sel:DWORD dst_unused:UNUSED_PAD src0_sel:DWORD src1_sel:WORD_1
	v_or_b32_sdwa v68, v74, v68 dst_sel:DWORD dst_unused:UNUSED_PAD src0_sel:DWORD src1_sel:WORD_1
	global_store_dwordx4 v[72:73], v[66:69], off nt
	ds_read_b32 v37, v49
	ds_read_b32 v74, v49 offset:1028
	ds_read_b32 v75, v49 offset:2056
	ds_read_b32 v76, v49 offset:3084
	ds_read_b32 v77, v49 offset:4112
	ds_read_b32 v78, v49 offset:5140
	ds_read_b32 v79, v49 offset:6168
	ds_read_b32 v80, v49 offset:7196
	v_add_u32_e32 v66, s8, v48
	v_lshlrev_b32_e32 v67, 1, v66
	v_and_b32_e32 v67, 0xffffffe0, v67
	v_add3_u32 v67, s1, v50, v67
	v_cndmask_b32_e32 v66, v67, v66, vcc
	v_ashrrev_i32_e32 v69, 31, v66
	v_mad_u64_u32 v[66:67], s[2:3], v66, s35, 0
	v_mov_b32_e32 v68, v67
	v_mad_u64_u32 v[68:69], s[2:3], v69, s35, v[68:69]
	v_mov_b32_e32 v67, v68
	v_lshl_add_u64 v[72:73], v[66:67], 1, v[70:71]
	s_waitcnt lgkmcnt(7)
	v_and_b32_sdwa v67, v37, v65 dst_sel:DWORD dst_unused:UNUSED_PAD src0_sel:WORD_1 src1_sel:DWORD
	v_add3_u32 v37, v37, v67, s41
	s_waitcnt lgkmcnt(4)
	v_and_b32_sdwa v67, v76, v65 dst_sel:DWORD dst_unused:UNUSED_PAD src0_sel:WORD_1 src1_sel:DWORD
	v_and_b32_sdwa v68, v74, v65 dst_sel:DWORD dst_unused:UNUSED_PAD src0_sel:WORD_1 src1_sel:DWORD
	v_and_b32_sdwa v66, v75, v65 dst_sel:DWORD dst_unused:UNUSED_PAD src0_sel:WORD_1 src1_sel:DWORD
	v_add3_u32 v67, v76, v67, s41
	v_add3_u32 v68, v74, v68, s41
	v_add3_u32 v66, v75, v66, s41
	v_and_b32_e32 v67, 0xffff0000, v67
	v_and_b32_e32 v68, 0xffff0000, v68
	s_waitcnt lgkmcnt(0)
	v_and_b32_sdwa v69, v80, v65 dst_sel:DWORD dst_unused:UNUSED_PAD src0_sel:WORD_1 src1_sel:DWORD
	v_and_b32_sdwa v74, v78, v65 dst_sel:DWORD dst_unused:UNUSED_PAD src0_sel:WORD_1 src1_sel:DWORD
	v_or_b32_sdwa v67, v67, v66 dst_sel:DWORD dst_unused:UNUSED_PAD src0_sel:DWORD src1_sel:WORD_1
	v_or_b32_sdwa v66, v68, v37 dst_sel:DWORD dst_unused:UNUSED_PAD src0_sel:DWORD src1_sel:WORD_1
	v_and_b32_sdwa v37, v79, v65 dst_sel:DWORD dst_unused:UNUSED_PAD src0_sel:WORD_1 src1_sel:DWORD
	v_and_b32_sdwa v68, v77, v65 dst_sel:DWORD dst_unused:UNUSED_PAD src0_sel:WORD_1 src1_sel:DWORD
	v_add3_u32 v69, v80, v69, s41
	v_add3_u32 v74, v78, v74, s41
	v_add3_u32 v68, v77, v68, s41
	v_add3_u32 v37, v79, v37, s41
	v_and_b32_e32 v69, 0xffff0000, v69
	v_and_b32_e32 v74, 0xffff0000, v74
	v_or_b32_sdwa v69, v69, v37 dst_sel:DWORD dst_unused:UNUSED_PAD src0_sel:DWORD src1_sel:WORD_1
	v_or_b32_sdwa v68, v74, v68 dst_sel:DWORD dst_unused:UNUSED_PAD src0_sel:DWORD src1_sel:WORD_1
	global_store_dwordx4 v[72:73], v[66:69], off nt
	ds_read_b32 v37, v52
	ds_read_b32 v74, v52 offset:1028
	ds_read_b32 v75, v52 offset:2056
	ds_read_b32 v76, v52 offset:3084
	ds_read_b32 v77, v52 offset:4112
	ds_read_b32 v78, v52 offset:5140
	ds_read_b32 v79, v52 offset:6168
	ds_read_b32 v80, v52 offset:7196
	v_add_u32_e32 v66, s8, v51
	v_lshlrev_b32_e32 v67, 1, v66
	v_and_b32_e32 v67, 0xffffffe0, v67
	v_add3_u32 v67, s1, v53, v67
	v_cndmask_b32_e32 v66, v67, v66, vcc
	v_ashrrev_i32_e32 v69, 31, v66
	v_mad_u64_u32 v[66:67], s[2:3], v66, s35, 0
	v_mov_b32_e32 v68, v67
	v_mad_u64_u32 v[68:69], s[2:3], v69, s35, v[68:69]
	v_mov_b32_e32 v67, v68
	v_lshl_add_u64 v[72:73], v[66:67], 1, v[70:71]
	s_waitcnt lgkmcnt(7)
	v_and_b32_sdwa v67, v37, v65 dst_sel:DWORD dst_unused:UNUSED_PAD src0_sel:WORD_1 src1_sel:DWORD
	v_add3_u32 v37, v37, v67, s41
	s_waitcnt lgkmcnt(4)
	v_and_b32_sdwa v67, v76, v65 dst_sel:DWORD dst_unused:UNUSED_PAD src0_sel:WORD_1 src1_sel:DWORD
	v_and_b32_sdwa v68, v74, v65 dst_sel:DWORD dst_unused:UNUSED_PAD src0_sel:WORD_1 src1_sel:DWORD
	v_and_b32_sdwa v66, v75, v65 dst_sel:DWORD dst_unused:UNUSED_PAD src0_sel:WORD_1 src1_sel:DWORD
	v_add3_u32 v67, v76, v67, s41
	v_add3_u32 v68, v74, v68, s41
	v_add3_u32 v66, v75, v66, s41
	v_and_b32_e32 v67, 0xffff0000, v67
	v_and_b32_e32 v68, 0xffff0000, v68
	s_waitcnt lgkmcnt(0)
	v_and_b32_sdwa v69, v80, v65 dst_sel:DWORD dst_unused:UNUSED_PAD src0_sel:WORD_1 src1_sel:DWORD
	v_and_b32_sdwa v74, v78, v65 dst_sel:DWORD dst_unused:UNUSED_PAD src0_sel:WORD_1 src1_sel:DWORD
	v_or_b32_sdwa v67, v67, v66 dst_sel:DWORD dst_unused:UNUSED_PAD src0_sel:DWORD src1_sel:WORD_1
	v_or_b32_sdwa v66, v68, v37 dst_sel:DWORD dst_unused:UNUSED_PAD src0_sel:DWORD src1_sel:WORD_1
	v_and_b32_sdwa v37, v79, v65 dst_sel:DWORD dst_unused:UNUSED_PAD src0_sel:WORD_1 src1_sel:DWORD
	v_and_b32_sdwa v68, v77, v65 dst_sel:DWORD dst_unused:UNUSED_PAD src0_sel:WORD_1 src1_sel:DWORD
	v_add3_u32 v69, v80, v69, s41
	v_add3_u32 v74, v78, v74, s41
	v_add3_u32 v68, v77, v68, s41
	v_add3_u32 v37, v79, v37, s41
	v_and_b32_e32 v69, 0xffff0000, v69
	v_and_b32_e32 v74, 0xffff0000, v74
	v_or_b32_sdwa v69, v69, v37 dst_sel:DWORD dst_unused:UNUSED_PAD src0_sel:DWORD src1_sel:WORD_1
	v_or_b32_sdwa v68, v74, v68 dst_sel:DWORD dst_unused:UNUSED_PAD src0_sel:DWORD src1_sel:WORD_1
	global_store_dwordx4 v[72:73], v[66:69], off nt
	ds_read_b32 v37, v55
	ds_read_b32 v72, v55 offset:1028
	ds_read_b32 v73, v55 offset:2056
	ds_read_b32 v74, v55 offset:3084
	ds_read_b32 v75, v55 offset:4112
	ds_read_b32 v76, v55 offset:5140
	ds_read_b32 v77, v55 offset:6168
	ds_read_b32 v78, v55 offset:7196
	v_add_u32_e32 v66, s8, v54
	v_lshlrev_b32_e32 v67, 1, v66
	v_and_b32_e32 v67, 0xffffffe0, v67
	v_add3_u32 v67, s1, v56, v67
	v_cndmask_b32_e32 v66, v67, v66, vcc
	v_ashrrev_i32_e32 v69, 31, v66
	v_mad_u64_u32 v[66:67], s[2:3], v66, s35, 0
	v_mov_b32_e32 v68, v67
	v_mad_u64_u32 v[68:69], s[2:3], v69, s35, v[68:69]
	v_mov_b32_e32 v67, v68
	v_lshl_add_u64 v[70:71], v[66:67], 1, v[70:71]
	s_waitcnt lgkmcnt(7)
	v_and_b32_sdwa v67, v37, v65 dst_sel:DWORD dst_unused:UNUSED_PAD src0_sel:WORD_1 src1_sel:DWORD
	v_add3_u32 v37, v37, v67, s41
	s_waitcnt lgkmcnt(4)
	v_and_b32_sdwa v67, v74, v65 dst_sel:DWORD dst_unused:UNUSED_PAD src0_sel:WORD_1 src1_sel:DWORD
	v_and_b32_sdwa v68, v72, v65 dst_sel:DWORD dst_unused:UNUSED_PAD src0_sel:WORD_1 src1_sel:DWORD
	v_and_b32_sdwa v66, v73, v65 dst_sel:DWORD dst_unused:UNUSED_PAD src0_sel:WORD_1 src1_sel:DWORD
	v_add3_u32 v67, v74, v67, s41
	v_add3_u32 v68, v72, v68, s41
	v_add3_u32 v66, v73, v66, s41
	v_and_b32_e32 v67, 0xffff0000, v67
	v_and_b32_e32 v68, 0xffff0000, v68
	s_waitcnt lgkmcnt(0)
	v_and_b32_sdwa v69, v78, v65 dst_sel:DWORD dst_unused:UNUSED_PAD src0_sel:WORD_1 src1_sel:DWORD
	v_and_b32_sdwa v72, v76, v65 dst_sel:DWORD dst_unused:UNUSED_PAD src0_sel:WORD_1 src1_sel:DWORD
	v_or_b32_sdwa v67, v67, v66 dst_sel:DWORD dst_unused:UNUSED_PAD src0_sel:DWORD src1_sel:WORD_1
	v_or_b32_sdwa v66, v68, v37 dst_sel:DWORD dst_unused:UNUSED_PAD src0_sel:DWORD src1_sel:WORD_1
	v_and_b32_sdwa v37, v77, v65 dst_sel:DWORD dst_unused:UNUSED_PAD src0_sel:WORD_1 src1_sel:DWORD
	v_and_b32_sdwa v68, v75, v65 dst_sel:DWORD dst_unused:UNUSED_PAD src0_sel:WORD_1 src1_sel:DWORD
	v_add3_u32 v69, v78, v69, s41
	v_add3_u32 v72, v76, v72, s41
	v_add3_u32 v68, v75, v68, s41
	v_add3_u32 v37, v77, v37, s41
	v_and_b32_e32 v69, 0xffff0000, v69
	v_and_b32_e32 v72, 0xffff0000, v72
	v_or_b32_sdwa v69, v69, v37 dst_sel:DWORD dst_unused:UNUSED_PAD src0_sel:DWORD src1_sel:WORD_1
	v_or_b32_sdwa v68, v72, v68 dst_sel:DWORD dst_unused:UNUSED_PAD src0_sel:DWORD src1_sel:WORD_1
	s_add_i32 s38, s38, s40
	s_add_i32 s39, s39, s40
	s_andn2_b64 vcc, exec, s[22:23]
	s_mov_b32 s1, s43
	s_mov_b32 s21, s10
	s_mov_b32 s8, s26
	s_mov_b32 s20, s30
	s_mov_b32 s35, s42
	s_mov_b64 s[2:3], s[24:25]
	global_store_dwordx4 v[70:71], v[66:69], off nt
	s_barrier
	s_cbranch_vccz .LBB0_2335

.LBB0_3747:
	s_waitcnt vmcnt(5)
	v_add_u32_e32 v2, 0x800, v34
	s_lshr_b32 s4, s8, 8
	v_ashrrev_i32_e32 v42, 6, v2
	v_cvt_f32_u32_e32 v2, s4
	s_sub_i32 s11, 0, s4
	s_abs_i32 s10, s9
	s_ashr_i32 s5, s9, 31
	v_rcp_iflag_f32_e32 v2, v2
	v_add_u32_e32 v3, 0xa00, v34
	v_ashrrev_i32_e32 v43, 6, v3
	v_add_u32_e32 v3, 0xc00, v34
	v_mul_f32_e32 v2, 0x4f7ffffe, v2
	v_cvt_u32_f32_e32 v2, v2
	v_lshlrev_b32_e32 v1, 2, v34
	v_ashrrev_i32_e32 v44, 6, v3
	v_add_u32_e32 v3, 0xe00, v34
	v_readfirstlane_b32 s12, v2
	s_mul_i32 s11, s11, s12
	s_mul_hi_u32 s11, s12, s11
	s_add_i32 s12, s12, s11
	s_mul_hi_u32 s11, s10, s12
	s_mul_i32 s12, s11, s4
	s_sub_i32 s10, s10, s12
	s_add_i32 s12, s11, 1
	s_sub_i32 s13, s10, s4
	s_cmp_ge_u32 s10, s4
	s_cselect_b32 s11, s12, s11
	s_cselect_b32 s10, s13, s10
	s_add_i32 s12, s11, 1
	s_cmp_ge_u32 s10, s4
	s_cselect_b32 s10, s12, s11
	s_xor_b32 s10, s10, s5
	s_sub_i32 s12, s10, s5
	s_mul_i32 s4, s12, s4
	s_sub_i32 s4, s9, s4
	s_lshl_b32 s4, s4, 8
	s_ashr_i32 s5, s4, 31
	s_lshl_b64 s[10:11], s[4:5], 2
	s_add_u32 s6, s6, s10
	v_and_b32_e32 v38, 0xfc, v1
	v_ashrrev_i32_e32 v45, 6, v3
	s_addc_u32 s7, s7, s11
	s_lshl_b32 s18, s12, 6
	v_mov_b32_e32 v37, 0
	v_lshlrev_b32_e32 v36, 2, v38
	v_add_u32_e32 v2, s18, v45
	v_lshl_add_u64 v[26:27], s[6:7], 0, v[36:37]
	v_ashrrev_i32_e32 v5, 31, v2
	v_mad_u64_u32 v[2:3], s[6:7], v2, s8, 0
	v_mov_b32_e32 v4, v3
	v_mad_u64_u32 v[4:5], s[6:7], v5, s8, v[4:5]
	v_mov_b32_e32 v3, v4
	v_lshl_add_u64 v[10:11], v[2:3], 2, v[26:27]
	v_add_u32_e32 v2, s18, v44
	v_ashrrev_i32_e32 v5, 31, v2
	v_mad_u64_u32 v[2:3], s[6:7], v2, s8, 0
	v_mov_b32_e32 v4, v3
	v_mad_u64_u32 v[4:5], s[6:7], v5, s8, v[4:5]
	v_mov_b32_e32 v3, v4
	v_lshl_add_u64 v[12:13], v[2:3], 2, v[26:27]
	global_load_dwordx4 v[6:9], v[10:11], off nt
	global_load_dwordx4 v[2:5], v[12:13], off nt
	v_add_u32_e32 v10, s18, v43
	v_ashrrev_i32_e32 v13, 31, v10
	v_mad_u64_u32 v[10:11], s[6:7], v10, s8, 0
	v_mov_b32_e32 v12, v11
	v_mad_u64_u32 v[12:13], s[6:7], v13, s8, v[12:13]
	v_mov_b32_e32 v11, v12
	v_lshl_add_u64 v[18:19], v[10:11], 2, v[26:27]
	v_add_u32_e32 v10, s18, v42
	v_ashrrev_i32_e32 v13, 31, v10
	v_mad_u64_u32 v[10:11], s[6:7], v10, s8, 0
	v_mov_b32_e32 v12, v11
	v_add_u32_e32 v55, 0x600, v34
	v_mad_u64_u32 v[12:13], s[6:7], v13, s8, v[12:13]
	v_ashrrev_i32_e32 v41, 6, v55
	v_mov_b32_e32 v11, v12
	v_lshl_add_u64 v[20:21], v[10:11], 2, v[26:27]
	global_load_dwordx4 v[14:17], v[18:19], off nt
	global_load_dwordx4 v[10:13], v[20:21], off nt
	v_add_u32_e32 v18, s18, v41
	v_ashrrev_i32_e32 v21, 31, v18
	v_mad_u64_u32 v[18:19], s[6:7], v18, s8, 0
	v_mov_b32_e32 v20, v19
	v_add_u32_e32 v52, 0x400, v34
	v_mad_u64_u32 v[20:21], s[6:7], v21, s8, v[20:21]
	v_ashrrev_i32_e32 v40, 6, v52
	v_mov_b32_e32 v19, v20
	v_lshl_add_u64 v[28:29], v[18:19], 2, v[26:27]
	v_add_u32_e32 v18, s18, v40
	v_ashrrev_i32_e32 v21, 31, v18
	v_mad_u64_u32 v[18:19], s[6:7], v18, s8, 0
	v_mov_b32_e32 v20, v19
	v_add_u32_e32 v39, 0x200, v34
	v_mad_u64_u32 v[20:21], s[6:7], v21, s8, v[20:21]
	v_ashrrev_i32_e32 v35, 6, v39
	v_mov_b32_e32 v19, v20
	s_waitcnt vmcnt(8)
	v_lshl_add_u64 v[30:31], v[18:19], 2, v[26:27]
	global_load_dwordx4 v[22:25], v[28:29], off nt
	global_load_dwordx4 v[18:21], v[30:31], off nt
	v_add_u32_e32 v28, s18, v35
	v_ashrrev_i32_e32 v31, 31, v28
	v_mad_u64_u32 v[28:29], s[6:7], v28, s8, 0
	v_mov_b32_e32 v30, v29
	v_mad_u64_u32 v[30:31], s[6:7], v31, s8, v[30:31]
	v_ashrrev_i32_e32 v1, 6, v34
	v_mov_b32_e32 v29, v30
	v_lshl_add_u64 v[46:47], v[28:29], 2, v[26:27]
	v_add_u32_e32 v28, s18, v1
	v_ashrrev_i32_e32 v31, 31, v28
	v_mad_u64_u32 v[28:29], s[6:7], v28, s8, 0
	v_mov_b32_e32 v30, v29
	v_mad_u64_u32 v[30:31], s[6:7], v31, s8, v[30:31]
	v_mov_b32_e32 v29, v30
	v_lshl_add_u64 v[48:49], v[28:29], 2, v[26:27]
	global_load_dwordx4 v[30:33], v[46:47], off nt
	global_load_dwordx4 v[26:29], v[48:49], off nt
	v_lshlrev_b32_e32 v46, 3, v34
	v_and_b32_e32 v66, 56, v46
	s_movk_i32 s5, 0x404
	v_readlane_b32 s16, v252, 3
	v_mad_u32_u24 v56, v66, s5, 0
	v_mul_lo_u32 v58, v1, s5
	v_mul_lo_u32 v59, v35, s5
	v_mul_lo_u32 v60, v40, s5
	v_mul_lo_u32 v61, v41, s5
	v_mul_lo_u32 v62, v42, s5
	v_mul_lo_u32 v63, v43, s5
	v_mul_lo_u32 v64, v44, s5
	v_mul_lo_u32 v65, v45, s5
	v_readlane_b32 s17, v252, 4
	s_add_u32 s5, s16, 0x1e940000
	s_addc_u32 s30, s17, 0
	s_add_u32 s8, s16, 0x16940000
	s_addc_u32 s9, s17, 0
	s_add_u32 s10, s78, 0x1000000
	s_addc_u32 s11, s79, 0
	s_add_u32 s12, s16, 0x16140000
	s_addc_u32 s13, s17, 0
	v_readlane_b32 s36, v250, 7
	s_add_u32 s31, s16, 0x15540000
	v_readlane_b32 s50, v250, 21
	v_readlane_b32 s51, v250, 22
	s_addc_u32 s33, s17, 0
	s_mov_b64 s[14:15], s[50:51]
	s_add_u32 s14, s14, 0x6c00000
	s_addc_u32 s15, s15, 0
	v_add_u32_e32 v36, 0, v36
	v_ashrrev_i32_e32 v46, 3, v34
	v_ashrrev_i32_e32 v49, 3, v39
	v_ashrrev_i32_e32 v52, 3, v52
	v_ashrrev_i32_e32 v55, 3, v55
	v_readlane_b32 s38, v250, 9
	s_add_u32 s16, s16, 0x11f40000
	s_mov_b32 s7, 0
	v_lshl_add_u32 v47, v46, 2, v56
	v_and_b32_e32 v48, 15, v46
	v_lshl_add_u32 v50, v49, 2, v56
	v_and_b32_e32 v51, 15, v49
	v_lshl_add_u32 v53, v52, 2, v56
	v_and_b32_e32 v54, 15, v52
	v_lshl_add_u32 v56, v55, 2, v56
	v_and_b32_e32 v57, 15, v55
	s_addc_u32 s17, s17, 0
	s_add_i32 s34, s20, 0x15e1
	s_mov_b32 s35, 17
	v_add_u32_e32 v58, v36, v58
	v_add_u32_e32 v59, v36, v59
	v_add_u32_e32 v60, v36, v60
	v_add_u32_e32 v61, v36, v61
	v_add_u32_e32 v62, v36, v62
	v_add_u32_e32 v63, v36, v63
	v_add_u32_e32 v64, v36, v64
	v_add_u32_e32 v65, v36, v65
	v_lshlrev_b32_e32 v36, 2, v38
	v_lshlrev_b32_e32 v38, 1, v66
	s_movk_i32 s36, 0x7fff
	v_mov_b32_e32 v66, 1
	s_mov_b32 s6, s19
	s_mov_b32 s38, s0
	s_mov_b64 s[22:23], s[2:3]
	v_readlane_b32 s37, v250, 8
	v_readlane_b32 s39, v250, 10
	v_readlane_b32 s40, v250, 11
	v_readlane_b32 s41, v250, 12
	v_readlane_b32 s42, v250, 13
	v_readlane_b32 s43, v250, 14
	v_readlane_b32 s44, v250, 15
	v_readlane_b32 s45, v250, 16
	v_readlane_b32 s46, v250, 17
	v_readlane_b32 s47, v250, 18
	v_readlane_b32 s48, v250, 19
	v_readlane_b32 s49, v250, 20
	s_branch .LBB0_3751

.LBB0_3749:
	s_lshr_b32 s24, s40, 8
	v_cvt_f32_u32_e32 v2, s24
	s_sub_i32 s29, 0, s24
	s_abs_i32 s28, s41
	s_ashr_i32 s25, s41, 31
	v_rcp_iflag_f32_e32 v2, v2
	s_nop 0
	v_mul_f32_e32 v2, 0x4f7ffffe, v2
	v_cvt_u32_f32_e32 v2, v2
	s_nop 0
	v_readfirstlane_b32 s42, v2
	s_mul_i32 s29, s29, s42
	s_mul_hi_u32 s29, s42, s29
	s_add_i32 s42, s42, s29
	s_mul_hi_u32 s29, s28, s42
	s_mul_i32 s42, s29, s24
	s_sub_i32 s28, s28, s42
	s_add_i32 s43, s29, 1
	s_sub_i32 s42, s28, s24
	s_cmp_ge_u32 s28, s24
	s_cselect_b32 s29, s43, s29
	s_cselect_b32 s28, s42, s28
	s_add_i32 s42, s29, 1
	s_cmp_ge_u32 s28, s24
	s_cselect_b32 s28, s42, s29
	s_xor_b32 s28, s28, s25
	s_sub_i32 s25, s28, s25
	s_lshl_b32 s29, s25, 6
	s_mul_i32 s25, s25, s24
	s_sub_i32 s24, s41, s25
	s_lshl_b32 s24, s24, 8
	s_ashr_i32 s25, s24, 31
	s_lshl_b64 s[42:43], s[24:25], 2
	s_add_u32 s26, s26, s42
	v_add_u32_e32 v4, s29, v1
	s_addc_u32 s27, s27, s43
	v_ashrrev_i32_e32 v7, 31, v4
	v_lshl_add_u64 v[2:3], s[26:27], 0, v[36:37]
	v_mad_u64_u32 v[4:5], s[26:27], v4, s40, 0
	v_mov_b32_e32 v6, v5
	v_mad_u64_u32 v[6:7], s[26:27], v7, s40, v[6:7]
	v_mov_b32_e32 v5, v6
	v_add_u32_e32 v6, s29, v35
	v_ashrrev_i32_e32 v9, 31, v6
	v_mad_u64_u32 v[6:7], s[26:27], v6, s40, 0
	v_mov_b32_e32 v8, v7
	v_mad_u64_u32 v[8:9], s[26:27], v9, s40, v[8:9]
	v_lshl_add_u64 v[4:5], v[4:5], 2, v[2:3]
	v_mov_b32_e32 v7, v8
	v_lshl_add_u64 v[6:7], v[6:7], 2, v[2:3]
	global_load_dwordx4 v[26:29], v[4:5], off nt
	global_load_dwordx4 v[30:33], v[6:7], off nt
	v_add_u32_e32 v4, s29, v40
	v_ashrrev_i32_e32 v7, 31, v4
	v_mad_u64_u32 v[4:5], s[26:27], v4, s40, 0
	v_mov_b32_e32 v6, v5
	v_mad_u64_u32 v[6:7], s[26:27], v7, s40, v[6:7]
	v_mov_b32_e32 v5, v6
	v_add_u32_e32 v6, s29, v41
	v_ashrrev_i32_e32 v9, 31, v6
	v_mad_u64_u32 v[6:7], s[26:27], v6, s40, 0
	v_mov_b32_e32 v8, v7
	v_mad_u64_u32 v[8:9], s[26:27], v9, s40, v[8:9]
	v_lshl_add_u64 v[4:5], v[4:5], 2, v[2:3]
	v_mov_b32_e32 v7, v8
	v_lshl_add_u64 v[6:7], v[6:7], 2, v[2:3]
	global_load_dwordx4 v[18:21], v[4:5], off nt
	global_load_dwordx4 v[22:25], v[6:7], off nt
	v_add_u32_e32 v4, s29, v42
	v_ashrrev_i32_e32 v7, 31, v4
	v_mad_u64_u32 v[4:5], s[26:27], v4, s40, 0
	v_mov_b32_e32 v6, v5
	v_mad_u64_u32 v[6:7], s[26:27], v7, s40, v[6:7]
	v_mov_b32_e32 v5, v6
	v_add_u32_e32 v6, s29, v43
	v_ashrrev_i32_e32 v9, 31, v6
	v_mad_u64_u32 v[6:7], s[26:27], v6, s40, 0
	v_mov_b32_e32 v8, v7
	v_mad_u64_u32 v[8:9], s[26:27], v9, s40, v[8:9]
	v_lshl_add_u64 v[4:5], v[4:5], 2, v[2:3]
	v_mov_b32_e32 v7, v8
	v_lshl_add_u64 v[6:7], v[6:7], 2, v[2:3]
	global_load_dwordx4 v[10:13], v[4:5], off nt
	global_load_dwordx4 v[14:17], v[6:7], off nt
	v_add_u32_e32 v4, s29, v44
	v_ashrrev_i32_e32 v7, 31, v4
	v_mad_u64_u32 v[4:5], s[26:27], v4, s40, 0
	v_mov_b32_e32 v6, v5
	v_mad_u64_u32 v[6:7], s[26:27], v7, s40, v[6:7]
	v_mov_b32_e32 v5, v6
	v_add_u32_e32 v6, s29, v45
	v_ashrrev_i32_e32 v9, 31, v6
	v_mad_u64_u32 v[6:7], s[26:27], v6, s40, 0
	v_mov_b32_e32 v8, v7
	v_mad_u64_u32 v[8:9], s[26:27], v9, s40, v[8:9]
	v_mov_b32_e32 v7, v8
	v_lshl_add_u64 v[4:5], v[4:5], 2, v[2:3]
	v_lshl_add_u64 v[6:7], v[6:7], 2, v[2:3]
	global_load_dwordx4 v[2:5], v[4:5], off nt
	s_nop 0
	global_load_dwordx4 v[6:9], v[6:7], off nt
.LBB0_3750:
	s_add_i32 s35, s35, -1
	s_cmp_eq_u32 s19, 0
	v_add_u32_e32 v67, s4, v46
	v_lshlrev_b32_e32 v39, 1, v67
	s_cselect_b64 vcc, -1, 0
	s_ashr_i32 s19, s18, 31
	v_and_b32_e32 v39, 0xffffffe0, v39
	s_lshl_b64 s[18:19], s[18:19], 1
	v_add3_u32 v68, s1, v48, v39
	s_add_u32 s2, s2, s18
	s_addc_u32 s3, s3, s19
	v_mov_b32_e32 v39, v37
	v_cndmask_b32_e32 v67, v68, v67, vcc
	v_lshl_add_u64 v[72:73], s[2:3], 0, v[38:39]
	v_mad_u64_u32 v[68:69], s[2:3], v67, s0, 0
	v_ashrrev_i32_e32 v71, 31, v67
	v_mov_b32_e32 v70, v69
	v_mad_u64_u32 v[70:71], s[2:3], v71, s0, v[70:71]
	ds_read_b32 v39, v47
	ds_read_b32 v76, v47 offset:1028
	ds_read_b32 v77, v47 offset:2056
	ds_read_b32 v78, v47 offset:3084
	ds_read_b32 v79, v47 offset:4112
	ds_read_b32 v80, v47 offset:5140
	ds_read_b32 v81, v47 offset:6168
	ds_read_b32 v82, v47 offset:7196
	v_mov_b32_e32 v69, v70
	v_lshl_add_u64 v[74:75], v[68:69], 1, v[72:73]
	s_waitcnt lgkmcnt(7)
	v_and_b32_sdwa v68, v39, v66 dst_sel:DWORD dst_unused:UNUSED_PAD src0_sel:WORD_1 src1_sel:DWORD
	v_add3_u32 v39, v39, v68, s36
	s_waitcnt lgkmcnt(4)
	v_and_b32_sdwa v68, v78, v66 dst_sel:DWORD dst_unused:UNUSED_PAD src0_sel:WORD_1 src1_sel:DWORD
	v_and_b32_sdwa v69, v76, v66 dst_sel:DWORD dst_unused:UNUSED_PAD src0_sel:WORD_1 src1_sel:DWORD
	v_and_b32_sdwa v67, v77, v66 dst_sel:DWORD dst_unused:UNUSED_PAD src0_sel:WORD_1 src1_sel:DWORD
	v_add3_u32 v68, v78, v68, s36
	v_add3_u32 v69, v76, v69, s36
	v_add3_u32 v67, v77, v67, s36
	v_and_b32_e32 v68, 0xffff0000, v68
	v_and_b32_e32 v70, 0xffff0000, v69
	v_or_b32_sdwa v69, v68, v67 dst_sel:DWORD dst_unused:UNUSED_PAD src0_sel:DWORD src1_sel:WORD_1
	v_or_b32_sdwa v68, v70, v39 dst_sel:DWORD dst_unused:UNUSED_PAD src0_sel:DWORD src1_sel:WORD_1
	s_waitcnt lgkmcnt(0)
	v_and_b32_sdwa v70, v82, v66 dst_sel:DWORD dst_unused:UNUSED_PAD src0_sel:WORD_1 src1_sel:DWORD
	v_and_b32_sdwa v71, v80, v66 dst_sel:DWORD dst_unused:UNUSED_PAD src0_sel:WORD_1 src1_sel:DWORD
	v_and_b32_sdwa v39, v81, v66 dst_sel:DWORD dst_unused:UNUSED_PAD src0_sel:WORD_1 src1_sel:DWORD
	v_and_b32_sdwa v67, v79, v66 dst_sel:DWORD dst_unused:UNUSED_PAD src0_sel:WORD_1 src1_sel:DWORD
	v_add3_u32 v70, v82, v70, s36
	v_add3_u32 v71, v80, v71, s36
	v_add3_u32 v67, v79, v67, s36
	v_add3_u32 v39, v81, v39, s36
	v_and_b32_e32 v70, 0xffff0000, v70
	v_and_b32_e32 v76, 0xffff0000, v71
	v_or_b32_sdwa v71, v70, v39 dst_sel:DWORD dst_unused:UNUSED_PAD src0_sel:DWORD src1_sel:WORD_1
	v_or_b32_sdwa v70, v76, v67 dst_sel:DWORD dst_unused:UNUSED_PAD src0_sel:DWORD src1_sel:WORD_1
	global_store_dwordx4 v[74:75], v[68:71], off nt
	ds_read_b32 v39, v50
	ds_read_b32 v67, v50 offset:1028
	ds_read_b32 v76, v50 offset:2056
	ds_read_b32 v77, v50 offset:3084
	ds_read_b32 v78, v50 offset:4112
	ds_read_b32 v79, v50 offset:5140
	ds_read_b32 v80, v50 offset:6168
	ds_read_b32 v81, v50 offset:7196
	v_add_u32_e32 v68, s4, v49
	v_lshlrev_b32_e32 v69, 1, v68
	v_and_b32_e32 v69, 0xffffffe0, v69
	v_add3_u32 v69, s1, v51, v69
	v_cndmask_b32_e32 v68, v69, v68, vcc
	v_ashrrev_i32_e32 v71, 31, v68
	v_mad_u64_u32 v[68:69], s[2:3], v68, s0, 0
	v_mov_b32_e32 v70, v69
	v_mad_u64_u32 v[70:71], s[2:3], v71, s0, v[70:71]
	v_mov_b32_e32 v69, v70
	v_lshl_add_u64 v[74:75], v[68:69], 1, v[72:73]
	s_waitcnt lgkmcnt(7)
	v_and_b32_sdwa v69, v39, v66 dst_sel:DWORD dst_unused:UNUSED_PAD src0_sel:WORD_1 src1_sel:DWORD
	v_add3_u32 v39, v39, v69, s36
	s_waitcnt lgkmcnt(4)
	v_and_b32_sdwa v69, v77, v66 dst_sel:DWORD dst_unused:UNUSED_PAD src0_sel:WORD_1 src1_sel:DWORD
	v_and_b32_sdwa v70, v67, v66 dst_sel:DWORD dst_unused:UNUSED_PAD src0_sel:WORD_1 src1_sel:DWORD
	v_and_b32_sdwa v68, v76, v66 dst_sel:DWORD dst_unused:UNUSED_PAD src0_sel:WORD_1 src1_sel:DWORD
	v_add3_u32 v69, v77, v69, s36
	v_add3_u32 v67, v67, v70, s36
	v_add3_u32 v68, v76, v68, s36
	v_and_b32_e32 v69, 0xffff0000, v69
	v_and_b32_e32 v67, 0xffff0000, v67
	s_waitcnt lgkmcnt(0)
	v_and_b32_sdwa v70, v81, v66 dst_sel:DWORD dst_unused:UNUSED_PAD src0_sel:WORD_1 src1_sel:DWORD
	v_and_b32_sdwa v71, v79, v66 dst_sel:DWORD dst_unused:UNUSED_PAD src0_sel:WORD_1 src1_sel:DWORD
	v_or_b32_sdwa v69, v69, v68 dst_sel:DWORD dst_unused:UNUSED_PAD src0_sel:DWORD src1_sel:WORD_1
	v_or_b32_sdwa v68, v67, v39 dst_sel:DWORD dst_unused:UNUSED_PAD src0_sel:DWORD src1_sel:WORD_1
	v_and_b32_sdwa v39, v80, v66 dst_sel:DWORD dst_unused:UNUSED_PAD src0_sel:WORD_1 src1_sel:DWORD
	v_and_b32_sdwa v67, v78, v66 dst_sel:DWORD dst_unused:UNUSED_PAD src0_sel:WORD_1 src1_sel:DWORD
	v_add3_u32 v70, v81, v70, s36
	v_add3_u32 v71, v79, v71, s36
	v_add3_u32 v67, v78, v67, s36
	v_add3_u32 v39, v80, v39, s36
	v_and_b32_e32 v70, 0xffff0000, v70
	v_and_b32_e32 v76, 0xffff0000, v71
	v_or_b32_sdwa v71, v70, v39 dst_sel:DWORD dst_unused:UNUSED_PAD src0_sel:DWORD src1_sel:WORD_1
	v_or_b32_sdwa v70, v76, v67 dst_sel:DWORD dst_unused:UNUSED_PAD src0_sel:DWORD src1_sel:WORD_1
	global_store_dwordx4 v[74:75], v[68:71], off nt
	ds_read_b32 v39, v53
	ds_read_b32 v67, v53 offset:1028
	ds_read_b32 v76, v53 offset:2056
	ds_read_b32 v77, v53 offset:3084
	ds_read_b32 v78, v53 offset:4112
	ds_read_b32 v79, v53 offset:5140
	ds_read_b32 v80, v53 offset:6168
	ds_read_b32 v81, v53 offset:7196
	v_add_u32_e32 v68, s4, v52
	v_lshlrev_b32_e32 v69, 1, v68
	v_and_b32_e32 v69, 0xffffffe0, v69
	v_add3_u32 v69, s1, v54, v69
	v_cndmask_b32_e32 v68, v69, v68, vcc
	v_ashrrev_i32_e32 v71, 31, v68
	v_mad_u64_u32 v[68:69], s[2:3], v68, s0, 0
	v_mov_b32_e32 v70, v69
	v_mad_u64_u32 v[70:71], s[2:3], v71, s0, v[70:71]
	v_mov_b32_e32 v69, v70
	v_lshl_add_u64 v[74:75], v[68:69], 1, v[72:73]
	s_waitcnt lgkmcnt(7)
	v_and_b32_sdwa v69, v39, v66 dst_sel:DWORD dst_unused:UNUSED_PAD src0_sel:WORD_1 src1_sel:DWORD
	v_add3_u32 v39, v39, v69, s36
	s_waitcnt lgkmcnt(4)
	v_and_b32_sdwa v69, v77, v66 dst_sel:DWORD dst_unused:UNUSED_PAD src0_sel:WORD_1 src1_sel:DWORD
	v_and_b32_sdwa v70, v67, v66 dst_sel:DWORD dst_unused:UNUSED_PAD src0_sel:WORD_1 src1_sel:DWORD
	v_and_b32_sdwa v68, v76, v66 dst_sel:DWORD dst_unused:UNUSED_PAD src0_sel:WORD_1 src1_sel:DWORD
	v_add3_u32 v69, v77, v69, s36
	v_add3_u32 v67, v67, v70, s36
	v_add3_u32 v68, v76, v68, s36
	v_and_b32_e32 v69, 0xffff0000, v69
	v_and_b32_e32 v67, 0xffff0000, v67
	s_waitcnt lgkmcnt(0)
	v_and_b32_sdwa v70, v81, v66 dst_sel:DWORD dst_unused:UNUSED_PAD src0_sel:WORD_1 src1_sel:DWORD
	v_and_b32_sdwa v71, v79, v66 dst_sel:DWORD dst_unused:UNUSED_PAD src0_sel:WORD_1 src1_sel:DWORD
	v_or_b32_sdwa v69, v69, v68 dst_sel:DWORD dst_unused:UNUSED_PAD src0_sel:DWORD src1_sel:WORD_1
	v_or_b32_sdwa v68, v67, v39 dst_sel:DWORD dst_unused:UNUSED_PAD src0_sel:DWORD src1_sel:WORD_1
	v_and_b32_sdwa v39, v80, v66 dst_sel:DWORD dst_unused:UNUSED_PAD src0_sel:WORD_1 src1_sel:DWORD
	v_and_b32_sdwa v67, v78, v66 dst_sel:DWORD dst_unused:UNUSED_PAD src0_sel:WORD_1 src1_sel:DWORD
	v_add3_u32 v70, v81, v70, s36
	v_add3_u32 v71, v79, v71, s36
	v_add3_u32 v67, v78, v67, s36
	v_add3_u32 v39, v80, v39, s36
	v_and_b32_e32 v70, 0xffff0000, v70
	v_and_b32_e32 v76, 0xffff0000, v71
	v_or_b32_sdwa v71, v70, v39 dst_sel:DWORD dst_unused:UNUSED_PAD src0_sel:DWORD src1_sel:WORD_1
	v_or_b32_sdwa v70, v76, v67 dst_sel:DWORD dst_unused:UNUSED_PAD src0_sel:DWORD src1_sel:WORD_1
	global_store_dwordx4 v[74:75], v[68:71], off nt
	ds_read_b32 v39, v56
	ds_read_b32 v67, v56 offset:1028
	ds_read_b32 v74, v56 offset:2056
	ds_read_b32 v75, v56 offset:3084
	ds_read_b32 v76, v56 offset:4112
	ds_read_b32 v77, v56 offset:5140
	ds_read_b32 v78, v56 offset:6168
	ds_read_b32 v79, v56 offset:7196
	v_add_u32_e32 v68, s4, v55
	v_lshlrev_b32_e32 v69, 1, v68
	v_and_b32_e32 v69, 0xffffffe0, v69
	v_add3_u32 v69, s1, v57, v69
	v_cndmask_b32_e32 v68, v69, v68, vcc
	v_ashrrev_i32_e32 v71, 31, v68
	v_mad_u64_u32 v[68:69], s[2:3], v68, s0, 0
	v_mov_b32_e32 v70, v69
	v_mad_u64_u32 v[70:71], s[0:1], v71, s0, v[70:71]
	v_mov_b32_e32 v69, v70
	v_lshl_add_u64 v[72:73], v[68:69], 1, v[72:73]
	s_waitcnt lgkmcnt(7)
	v_and_b32_sdwa v69, v39, v66 dst_sel:DWORD dst_unused:UNUSED_PAD src0_sel:WORD_1 src1_sel:DWORD
	v_add3_u32 v39, v39, v69, s36
	s_waitcnt lgkmcnt(4)
	v_and_b32_sdwa v69, v75, v66 dst_sel:DWORD dst_unused:UNUSED_PAD src0_sel:WORD_1 src1_sel:DWORD
	v_and_b32_sdwa v70, v67, v66 dst_sel:DWORD dst_unused:UNUSED_PAD src0_sel:WORD_1 src1_sel:DWORD
	v_and_b32_sdwa v68, v74, v66 dst_sel:DWORD dst_unused:UNUSED_PAD src0_sel:WORD_1 src1_sel:DWORD
	v_add3_u32 v69, v75, v69, s36
	v_add3_u32 v67, v67, v70, s36
	v_add3_u32 v68, v74, v68, s36
	v_and_b32_e32 v69, 0xffff0000, v69
	v_and_b32_e32 v67, 0xffff0000, v67
	s_waitcnt lgkmcnt(0)
	v_and_b32_sdwa v70, v79, v66 dst_sel:DWORD dst_unused:UNUSED_PAD src0_sel:WORD_1 src1_sel:DWORD
	v_and_b32_sdwa v71, v77, v66 dst_sel:DWORD dst_unused:UNUSED_PAD src0_sel:WORD_1 src1_sel:DWORD
	v_or_b32_sdwa v69, v69, v68 dst_sel:DWORD dst_unused:UNUSED_PAD src0_sel:DWORD src1_sel:WORD_1
	v_or_b32_sdwa v68, v67, v39 dst_sel:DWORD dst_unused:UNUSED_PAD src0_sel:DWORD src1_sel:WORD_1
	v_and_b32_sdwa v39, v78, v66 dst_sel:DWORD dst_unused:UNUSED_PAD src0_sel:WORD_1 src1_sel:DWORD
	v_and_b32_sdwa v67, v76, v66 dst_sel:DWORD dst_unused:UNUSED_PAD src0_sel:WORD_1 src1_sel:DWORD
	v_add3_u32 v70, v79, v70, s36
	v_add3_u32 v71, v77, v71, s36
	v_add3_u32 v67, v76, v67, s36
	v_add3_u32 v39, v78, v39, s36
	v_and_b32_e32 v70, 0xffff0000, v70
	v_and_b32_e32 v74, 0xffff0000, v71
	v_or_b32_sdwa v71, v70, v39 dst_sel:DWORD dst_unused:UNUSED_PAD src0_sel:DWORD src1_sel:WORD_1
	v_or_b32_sdwa v70, v74, v67 dst_sel:DWORD dst_unused:UNUSED_PAD src0_sel:DWORD src1_sel:WORD_1
	s_add_i32 s34, s34, 1
	s_and_b64 vcc, exec, s[20:21]
	s_mov_b32 s28, s37
	s_mov_b32 s1, s39
	s_mov_b32 s19, s6
	s_mov_b32 s4, s24
	s_mov_b32 s18, s29
	s_mov_b32 s0, s38
	s_mov_b64 s[2:3], s[22:23]
	global_store_dwordx4 v[72:73], v[68:71], off nt
	s_barrier
	s_cbranch_vccnz .LBB0_3769

.LBB0_3796:
	s_waitcnt vmcnt(5)
	v_add_u32_e32 v2, 0x800, v34
	s_lshr_b32 s0, s8, 8
	v_ashrrev_i32_e32 v42, 6, v2
	v_cvt_f32_u32_e32 v2, s0
	s_sub_i32 s10, 0, s0
	s_abs_i32 s5, s9
	s_ashr_i32 s4, s9, 31
	v_rcp_iflag_f32_e32 v2, v2
	v_add_u32_e32 v3, 0xa00, v34
	v_ashrrev_i32_e32 v43, 6, v3
	v_add_u32_e32 v3, 0xc00, v34
	v_mul_f32_e32 v2, 0x4f7ffffe, v2
	v_cvt_u32_f32_e32 v2, v2
	v_lshlrev_b32_e32 v1, 2, v34
	v_ashrrev_i32_e32 v44, 6, v3
	v_add_u32_e32 v3, 0xe00, v34
	v_readfirstlane_b32 s11, v2
	s_mul_i32 s10, s10, s11
	s_mul_hi_u32 s10, s11, s10
	s_add_i32 s11, s11, s10
	s_mul_hi_u32 s10, s5, s11
	s_mul_i32 s11, s10, s0
	s_sub_i32 s5, s5, s11
	s_add_i32 s11, s10, 1
	s_sub_i32 s12, s5, s0
	s_cmp_ge_u32 s5, s0
	s_cselect_b32 s10, s11, s10
	s_cselect_b32 s5, s12, s5
	s_add_i32 s11, s10, 1
	s_cmp_ge_u32 s5, s0
	s_cselect_b32 s5, s11, s10
	s_xor_b32 s5, s5, s4
	s_sub_i32 s12, s5, s4
	s_mul_i32 s0, s12, s0
	s_sub_i32 s0, s9, s0
	s_lshl_b32 s4, s0, 8
	s_ashr_i32 s5, s4, 31
	s_lshl_b64 s[10:11], s[4:5], 2
	s_add_u32 s6, s6, s10
	v_and_b32_e32 v38, 0xfc, v1
	v_ashrrev_i32_e32 v45, 6, v3
	s_addc_u32 s7, s7, s11
	s_lshl_b32 s18, s12, 6
	v_mov_b32_e32 v37, 0
	v_lshlrev_b32_e32 v36, 2, v38
	v_add_u32_e32 v2, s18, v45
	v_lshl_add_u64 v[26:27], s[6:7], 0, v[36:37]
	v_ashrrev_i32_e32 v5, 31, v2
	v_mad_u64_u32 v[2:3], s[6:7], v2, s8, 0
	v_mov_b32_e32 v4, v3
	v_mad_u64_u32 v[4:5], s[6:7], v5, s8, v[4:5]
	v_mov_b32_e32 v3, v4
	v_lshl_add_u64 v[10:11], v[2:3], 2, v[26:27]
	v_add_u32_e32 v2, s18, v44
	v_ashrrev_i32_e32 v5, 31, v2
	v_mad_u64_u32 v[2:3], s[6:7], v2, s8, 0
	v_mov_b32_e32 v4, v3
	v_mad_u64_u32 v[4:5], s[6:7], v5, s8, v[4:5]
	v_mov_b32_e32 v3, v4
	v_lshl_add_u64 v[12:13], v[2:3], 2, v[26:27]
	global_load_dwordx4 v[6:9], v[10:11], off nt
	global_load_dwordx4 v[2:5], v[12:13], off nt
	v_add_u32_e32 v10, s18, v43
	v_ashrrev_i32_e32 v13, 31, v10
	v_mad_u64_u32 v[10:11], s[6:7], v10, s8, 0
	v_mov_b32_e32 v12, v11
	v_mad_u64_u32 v[12:13], s[6:7], v13, s8, v[12:13]
	v_mov_b32_e32 v11, v12
	v_lshl_add_u64 v[18:19], v[10:11], 2, v[26:27]
	v_add_u32_e32 v10, s18, v42
	v_ashrrev_i32_e32 v13, 31, v10
	v_mad_u64_u32 v[10:11], s[6:7], v10, s8, 0
	v_mov_b32_e32 v12, v11
	v_add_u32_e32 v55, 0x600, v34
	v_mad_u64_u32 v[12:13], s[6:7], v13, s8, v[12:13]
	v_ashrrev_i32_e32 v41, 6, v55
	v_mov_b32_e32 v11, v12
	v_lshl_add_u64 v[20:21], v[10:11], 2, v[26:27]
	global_load_dwordx4 v[14:17], v[18:19], off nt
	global_load_dwordx4 v[10:13], v[20:21], off nt
	v_add_u32_e32 v18, s18, v41
	v_ashrrev_i32_e32 v21, 31, v18
	v_mad_u64_u32 v[18:19], s[6:7], v18, s8, 0
	v_mov_b32_e32 v20, v19
	v_add_u32_e32 v52, 0x400, v34
	v_mad_u64_u32 v[20:21], s[6:7], v21, s8, v[20:21]
	v_ashrrev_i32_e32 v40, 6, v52
	v_mov_b32_e32 v19, v20
	v_lshl_add_u64 v[28:29], v[18:19], 2, v[26:27]
	v_add_u32_e32 v18, s18, v40
	v_ashrrev_i32_e32 v21, 31, v18
	v_mad_u64_u32 v[18:19], s[6:7], v18, s8, 0
	v_mov_b32_e32 v20, v19
	v_add_u32_e32 v35, 0x200, v34
	v_mad_u64_u32 v[20:21], s[6:7], v21, s8, v[20:21]
	v_ashrrev_i32_e32 v39, 6, v35
	v_mov_b32_e32 v19, v20
	s_waitcnt vmcnt(8)
	v_lshl_add_u64 v[30:31], v[18:19], 2, v[26:27]
	global_load_dwordx4 v[22:25], v[28:29], off nt
	global_load_dwordx4 v[18:21], v[30:31], off nt
	v_add_u32_e32 v28, s18, v39
	v_ashrrev_i32_e32 v31, 31, v28
	v_mad_u64_u32 v[28:29], s[6:7], v28, s8, 0
	v_mov_b32_e32 v30, v29
	v_mad_u64_u32 v[30:31], s[6:7], v31, s8, v[30:31]
	v_ashrrev_i32_e32 v1, 6, v34
	v_mov_b32_e32 v29, v30
	v_lshl_add_u64 v[46:47], v[28:29], 2, v[26:27]
	v_add_u32_e32 v28, s18, v1
	v_ashrrev_i32_e32 v31, 31, v28
	v_mad_u64_u32 v[28:29], s[6:7], v28, s8, 0
	v_mov_b32_e32 v30, v29
	v_mad_u64_u32 v[30:31], s[6:7], v31, s8, v[30:31]
	v_mov_b32_e32 v29, v30
	v_lshl_add_u64 v[48:49], v[28:29], 2, v[26:27]
	global_load_dwordx4 v[30:33], v[46:47], off nt
	global_load_dwordx4 v[26:29], v[48:49], off nt
	v_lshlrev_b32_e32 v46, 3, v34
	v_and_b32_e32 v66, 56, v46
	s_movk_i32 s0, 0x404
	v_readlane_b32 s16, v252, 3
	v_mad_u32_u24 v56, v66, s0, 0
	v_mul_lo_u32 v58, v1, s0
	v_mul_lo_u32 v59, v39, s0
	v_mul_lo_u32 v60, v40, s0
	v_mul_lo_u32 v61, v41, s0
	v_mul_lo_u32 v62, v42, s0
	v_mul_lo_u32 v63, v43, s0
	v_mul_lo_u32 v64, v44, s0
	v_mul_lo_u32 v65, v45, s0
	v_readlane_b32 s17, v252, 4
	s_add_u32 s0, s16, 0x1e940000
	s_addc_u32 s5, s17, 0
	s_add_u32 s8, s16, 0x16940000
	s_addc_u32 s9, s17, 0
	s_add_u32 s10, s78, 0x1000000
	s_addc_u32 s11, s79, 0
	s_add_u32 s12, s16, 0x16140000
	s_addc_u32 s13, s17, 0
	v_readlane_b32 s36, v250, 7
	s_add_u32 s31, s16, 0x15540000
	v_readlane_b32 s50, v250, 21
	v_readlane_b32 s51, v250, 22
	s_addc_u32 s33, s17, 0
	s_mov_b64 s[14:15], s[50:51]
	s_add_u32 s14, s14, 0x6c00000
	s_addc_u32 s15, s15, 0
	v_add_u32_e32 v36, 0, v36
	v_ashrrev_i32_e32 v46, 3, v34
	v_ashrrev_i32_e32 v49, 3, v35
	v_ashrrev_i32_e32 v52, 3, v52
	v_ashrrev_i32_e32 v55, 3, v55
	v_readlane_b32 s38, v250, 9
	s_add_u32 s16, s16, 0x11f40000
	s_mov_b32 s7, 0
	v_lshl_add_u32 v47, v46, 2, v56
	v_and_b32_e32 v48, 15, v46
	v_lshl_add_u32 v50, v49, 2, v56
	v_and_b32_e32 v51, 15, v49
	v_lshl_add_u32 v53, v52, 2, v56
	v_and_b32_e32 v54, 15, v52
	v_lshl_add_u32 v56, v55, 2, v56
	v_and_b32_e32 v57, 15, v55
	s_addc_u32 s17, s17, 0
	s_add_i32 s34, s20, 0xfffffce1
	s_mov_b32 s35, 25
	v_add_u32_e32 v58, v36, v58
	v_add_u32_e32 v59, v36, v59
	v_add_u32_e32 v60, v36, v60
	v_add_u32_e32 v61, v36, v61
	v_add_u32_e32 v62, v36, v62
	v_add_u32_e32 v63, v36, v63
	v_add_u32_e32 v64, v36, v64
	v_add_u32_e32 v65, v36, v65
	v_lshlrev_b32_e32 v36, 2, v38
	v_lshlrev_b32_e32 v34, 1, v66
	s_movk_i32 s36, 0x7fff
	v_mov_b32_e32 v38, 1
	s_mov_b32 s6, s19
	s_mov_b32 s38, s30
	s_mov_b64 s[22:23], s[2:3]
	v_readlane_b32 s37, v250, 8
	v_readlane_b32 s39, v250, 10
	v_readlane_b32 s40, v250, 11
	v_readlane_b32 s41, v250, 12
	v_readlane_b32 s42, v250, 13
	v_readlane_b32 s43, v250, 14
	v_readlane_b32 s44, v250, 15
	v_readlane_b32 s45, v250, 16
	v_readlane_b32 s46, v250, 17
	v_readlane_b32 s47, v250, 18
	v_readlane_b32 s48, v250, 19
	v_readlane_b32 s49, v250, 20
	s_branch .LBB0_3800

.LBB0_3798:
	s_lshr_b32 s24, s40, 8
	v_cvt_f32_u32_e32 v2, s24
	s_sub_i32 s29, 0, s24
	s_abs_i32 s28, s41
	s_ashr_i32 s25, s41, 31
	v_rcp_iflag_f32_e32 v2, v2
	s_nop 0
	v_mul_f32_e32 v2, 0x4f7ffffe, v2
	v_cvt_u32_f32_e32 v2, v2
	s_nop 0
	v_readfirstlane_b32 s42, v2
	s_mul_i32 s29, s29, s42
	s_mul_hi_u32 s29, s42, s29
	s_add_i32 s42, s42, s29
	s_mul_hi_u32 s29, s28, s42
	s_mul_i32 s42, s29, s24
	s_sub_i32 s28, s28, s42
	s_add_i32 s43, s29, 1
	s_sub_i32 s42, s28, s24
	s_cmp_ge_u32 s28, s24
	s_cselect_b32 s29, s43, s29
	s_cselect_b32 s28, s42, s28
	s_add_i32 s42, s29, 1
	s_cmp_ge_u32 s28, s24
	s_cselect_b32 s28, s42, s29
	s_xor_b32 s28, s28, s25
	s_sub_i32 s25, s28, s25
	s_lshl_b32 s29, s25, 6
	s_mul_i32 s25, s25, s24
	s_sub_i32 s24, s41, s25
	s_lshl_b32 s24, s24, 8
	s_ashr_i32 s25, s24, 31
	s_lshl_b64 s[42:43], s[24:25], 2
	s_add_u32 s26, s26, s42
	v_add_u32_e32 v4, s29, v1
	s_addc_u32 s27, s27, s43
	v_ashrrev_i32_e32 v7, 31, v4
	v_lshl_add_u64 v[2:3], s[26:27], 0, v[36:37]
	v_mad_u64_u32 v[4:5], s[26:27], v4, s40, 0
	v_mov_b32_e32 v6, v5
	v_mad_u64_u32 v[6:7], s[26:27], v7, s40, v[6:7]
	v_mov_b32_e32 v5, v6
	v_add_u32_e32 v6, s29, v39
	v_ashrrev_i32_e32 v9, 31, v6
	v_mad_u64_u32 v[6:7], s[26:27], v6, s40, 0
	v_mov_b32_e32 v8, v7
	v_mad_u64_u32 v[8:9], s[26:27], v9, s40, v[8:9]
	v_lshl_add_u64 v[4:5], v[4:5], 2, v[2:3]
	v_mov_b32_e32 v7, v8
	v_lshl_add_u64 v[6:7], v[6:7], 2, v[2:3]
	global_load_dwordx4 v[26:29], v[4:5], off nt
	global_load_dwordx4 v[30:33], v[6:7], off nt
	v_add_u32_e32 v4, s29, v40
	v_ashrrev_i32_e32 v7, 31, v4
	v_mad_u64_u32 v[4:5], s[26:27], v4, s40, 0
	v_mov_b32_e32 v6, v5
	v_mad_u64_u32 v[6:7], s[26:27], v7, s40, v[6:7]
	v_mov_b32_e32 v5, v6
	v_add_u32_e32 v6, s29, v41
	v_ashrrev_i32_e32 v9, 31, v6
	v_mad_u64_u32 v[6:7], s[26:27], v6, s40, 0
	v_mov_b32_e32 v8, v7
	v_mad_u64_u32 v[8:9], s[26:27], v9, s40, v[8:9]
	v_lshl_add_u64 v[4:5], v[4:5], 2, v[2:3]
	v_mov_b32_e32 v7, v8
	v_lshl_add_u64 v[6:7], v[6:7], 2, v[2:3]
	global_load_dwordx4 v[18:21], v[4:5], off nt
	global_load_dwordx4 v[22:25], v[6:7], off nt
	v_add_u32_e32 v4, s29, v42
	v_ashrrev_i32_e32 v7, 31, v4
	v_mad_u64_u32 v[4:5], s[26:27], v4, s40, 0
	v_mov_b32_e32 v6, v5
	v_mad_u64_u32 v[6:7], s[26:27], v7, s40, v[6:7]
	v_mov_b32_e32 v5, v6
	v_add_u32_e32 v6, s29, v43
	v_ashrrev_i32_e32 v9, 31, v6
	v_mad_u64_u32 v[6:7], s[26:27], v6, s40, 0
	v_mov_b32_e32 v8, v7
	v_mad_u64_u32 v[8:9], s[26:27], v9, s40, v[8:9]
	v_lshl_add_u64 v[4:5], v[4:5], 2, v[2:3]
	v_mov_b32_e32 v7, v8
	v_lshl_add_u64 v[6:7], v[6:7], 2, v[2:3]
	global_load_dwordx4 v[10:13], v[4:5], off nt
	global_load_dwordx4 v[14:17], v[6:7], off nt
	v_add_u32_e32 v4, s29, v44
	v_ashrrev_i32_e32 v7, 31, v4
	v_mad_u64_u32 v[4:5], s[26:27], v4, s40, 0
	v_mov_b32_e32 v6, v5
	v_mad_u64_u32 v[6:7], s[26:27], v7, s40, v[6:7]
	v_mov_b32_e32 v5, v6
	v_add_u32_e32 v6, s29, v45
	v_ashrrev_i32_e32 v9, 31, v6
	v_mad_u64_u32 v[6:7], s[26:27], v6, s40, 0
	v_mov_b32_e32 v8, v7
	v_mad_u64_u32 v[8:9], s[26:27], v9, s40, v[8:9]
	v_mov_b32_e32 v7, v8
	v_lshl_add_u64 v[4:5], v[4:5], 2, v[2:3]
	v_lshl_add_u64 v[6:7], v[6:7], 2, v[2:3]
	global_load_dwordx4 v[2:5], v[4:5], off nt
	s_nop 0
	global_load_dwordx4 v[6:9], v[6:7], off nt
.LBB0_3799:
	s_add_i32 s35, s35, -1
	s_cmp_eq_u32 s19, 0
	v_add_u32_e32 v66, s4, v46
	v_lshlrev_b32_e32 v35, 1, v66
	s_cselect_b64 vcc, -1, 0
	s_ashr_i32 s19, s18, 31
	v_and_b32_e32 v35, 0xffffffe0, v35
	s_lshl_b64 s[18:19], s[18:19], 1
	v_add3_u32 v67, s1, v48, v35
	s_add_u32 s2, s2, s18
	s_addc_u32 s3, s3, s19
	v_mov_b32_e32 v35, v37
	v_cndmask_b32_e32 v66, v67, v66, vcc
	v_lshl_add_u64 v[70:71], s[2:3], 0, v[34:35]
	v_ashrrev_i32_e32 v69, 31, v66
	v_mad_u64_u32 v[66:67], s[2:3], v66, s30, 0
	v_mov_b32_e32 v68, v67
	ds_read_b32 v35, v47
	ds_read_b32 v74, v47 offset:1028
	ds_read_b32 v75, v47 offset:2056
	ds_read_b32 v76, v47 offset:3084
	ds_read_b32 v77, v47 offset:4112
	ds_read_b32 v78, v47 offset:5140
	ds_read_b32 v79, v47 offset:6168
	ds_read_b32 v80, v47 offset:7196
	v_mad_u64_u32 v[68:69], s[2:3], v69, s30, v[68:69]
	v_mov_b32_e32 v67, v68
	v_lshl_add_u64 v[72:73], v[66:67], 1, v[70:71]
	s_waitcnt lgkmcnt(7)
	v_and_b32_sdwa v67, v35, v38 dst_sel:DWORD dst_unused:UNUSED_PAD src0_sel:WORD_1 src1_sel:DWORD
	v_add3_u32 v35, v35, v67, s36
	s_waitcnt lgkmcnt(4)
	v_and_b32_sdwa v67, v76, v38 dst_sel:DWORD dst_unused:UNUSED_PAD src0_sel:WORD_1 src1_sel:DWORD
	v_and_b32_sdwa v68, v74, v38 dst_sel:DWORD dst_unused:UNUSED_PAD src0_sel:WORD_1 src1_sel:DWORD
	v_and_b32_sdwa v66, v75, v38 dst_sel:DWORD dst_unused:UNUSED_PAD src0_sel:WORD_1 src1_sel:DWORD
	v_add3_u32 v67, v76, v67, s36
	v_add3_u32 v68, v74, v68, s36
	v_add3_u32 v66, v75, v66, s36
	v_and_b32_e32 v67, 0xffff0000, v67
	v_and_b32_e32 v68, 0xffff0000, v68
	s_waitcnt lgkmcnt(0)
	v_and_b32_sdwa v69, v80, v38 dst_sel:DWORD dst_unused:UNUSED_PAD src0_sel:WORD_1 src1_sel:DWORD
	v_and_b32_sdwa v74, v78, v38 dst_sel:DWORD dst_unused:UNUSED_PAD src0_sel:WORD_1 src1_sel:DWORD
	v_or_b32_sdwa v67, v67, v66 dst_sel:DWORD dst_unused:UNUSED_PAD src0_sel:DWORD src1_sel:WORD_1
	v_or_b32_sdwa v66, v68, v35 dst_sel:DWORD dst_unused:UNUSED_PAD src0_sel:DWORD src1_sel:WORD_1
	v_and_b32_sdwa v35, v79, v38 dst_sel:DWORD dst_unused:UNUSED_PAD src0_sel:WORD_1 src1_sel:DWORD
	v_and_b32_sdwa v68, v77, v38 dst_sel:DWORD dst_unused:UNUSED_PAD src0_sel:WORD_1 src1_sel:DWORD
	v_add3_u32 v69, v80, v69, s36
	v_add3_u32 v74, v78, v74, s36
	v_add3_u32 v68, v77, v68, s36
	v_add3_u32 v35, v79, v35, s36
	v_and_b32_e32 v69, 0xffff0000, v69
	v_and_b32_e32 v74, 0xffff0000, v74
	v_or_b32_sdwa v69, v69, v35 dst_sel:DWORD dst_unused:UNUSED_PAD src0_sel:DWORD src1_sel:WORD_1
	v_or_b32_sdwa v68, v74, v68 dst_sel:DWORD dst_unused:UNUSED_PAD src0_sel:DWORD src1_sel:WORD_1
	global_store_dwordx4 v[72:73], v[66:69], off nt
	ds_read_b32 v35, v50
	ds_read_b32 v74, v50 offset:1028
	ds_read_b32 v75, v50 offset:2056
	ds_read_b32 v76, v50 offset:3084
	ds_read_b32 v77, v50 offset:4112
	ds_read_b32 v78, v50 offset:5140
	ds_read_b32 v79, v50 offset:6168
	ds_read_b32 v80, v50 offset:7196
	v_add_u32_e32 v66, s4, v49
	v_lshlrev_b32_e32 v67, 1, v66
	v_and_b32_e32 v67, 0xffffffe0, v67
	v_add3_u32 v67, s1, v51, v67
	v_cndmask_b32_e32 v66, v67, v66, vcc
	v_ashrrev_i32_e32 v69, 31, v66
	v_mad_u64_u32 v[66:67], s[2:3], v66, s30, 0
	v_mov_b32_e32 v68, v67
	v_mad_u64_u32 v[68:69], s[2:3], v69, s30, v[68:69]
	v_mov_b32_e32 v67, v68
	v_lshl_add_u64 v[72:73], v[66:67], 1, v[70:71]
	s_waitcnt lgkmcnt(7)
	v_and_b32_sdwa v67, v35, v38 dst_sel:DWORD dst_unused:UNUSED_PAD src0_sel:WORD_1 src1_sel:DWORD
	v_add3_u32 v35, v35, v67, s36
	s_waitcnt lgkmcnt(4)
	v_and_b32_sdwa v67, v76, v38 dst_sel:DWORD dst_unused:UNUSED_PAD src0_sel:WORD_1 src1_sel:DWORD
	v_and_b32_sdwa v68, v74, v38 dst_sel:DWORD dst_unused:UNUSED_PAD src0_sel:WORD_1 src1_sel:DWORD
	v_and_b32_sdwa v66, v75, v38 dst_sel:DWORD dst_unused:UNUSED_PAD src0_sel:WORD_1 src1_sel:DWORD
	v_add3_u32 v67, v76, v67, s36
	v_add3_u32 v68, v74, v68, s36
	v_add3_u32 v66, v75, v66, s36
	v_and_b32_e32 v67, 0xffff0000, v67
	v_and_b32_e32 v68, 0xffff0000, v68
	s_waitcnt lgkmcnt(0)
	v_and_b32_sdwa v69, v80, v38 dst_sel:DWORD dst_unused:UNUSED_PAD src0_sel:WORD_1 src1_sel:DWORD
	v_and_b32_sdwa v74, v78, v38 dst_sel:DWORD dst_unused:UNUSED_PAD src0_sel:WORD_1 src1_sel:DWORD
	v_or_b32_sdwa v67, v67, v66 dst_sel:DWORD dst_unused:UNUSED_PAD src0_sel:DWORD src1_sel:WORD_1
	v_or_b32_sdwa v66, v68, v35 dst_sel:DWORD dst_unused:UNUSED_PAD src0_sel:DWORD src1_sel:WORD_1
	v_and_b32_sdwa v35, v79, v38 dst_sel:DWORD dst_unused:UNUSED_PAD src0_sel:WORD_1 src1_sel:DWORD
	v_and_b32_sdwa v68, v77, v38 dst_sel:DWORD dst_unused:UNUSED_PAD src0_sel:WORD_1 src1_sel:DWORD
	v_add3_u32 v69, v80, v69, s36
	v_add3_u32 v74, v78, v74, s36
	v_add3_u32 v68, v77, v68, s36
	v_add3_u32 v35, v79, v35, s36
	v_and_b32_e32 v69, 0xffff0000, v69
	v_and_b32_e32 v74, 0xffff0000, v74
	v_or_b32_sdwa v69, v69, v35 dst_sel:DWORD dst_unused:UNUSED_PAD src0_sel:DWORD src1_sel:WORD_1
	v_or_b32_sdwa v68, v74, v68 dst_sel:DWORD dst_unused:UNUSED_PAD src0_sel:DWORD src1_sel:WORD_1
	global_store_dwordx4 v[72:73], v[66:69], off nt
	ds_read_b32 v35, v53
	ds_read_b32 v74, v53 offset:1028
	ds_read_b32 v75, v53 offset:2056
	ds_read_b32 v76, v53 offset:3084
	ds_read_b32 v77, v53 offset:4112
	ds_read_b32 v78, v53 offset:5140
	ds_read_b32 v79, v53 offset:6168
	ds_read_b32 v80, v53 offset:7196
	v_add_u32_e32 v66, s4, v52
	v_lshlrev_b32_e32 v67, 1, v66
	v_and_b32_e32 v67, 0xffffffe0, v67
	v_add3_u32 v67, s1, v54, v67
	v_cndmask_b32_e32 v66, v67, v66, vcc
	v_ashrrev_i32_e32 v69, 31, v66
	v_mad_u64_u32 v[66:67], s[2:3], v66, s30, 0
	v_mov_b32_e32 v68, v67
	v_mad_u64_u32 v[68:69], s[2:3], v69, s30, v[68:69]
	v_mov_b32_e32 v67, v68
	v_lshl_add_u64 v[72:73], v[66:67], 1, v[70:71]
	s_waitcnt lgkmcnt(7)
	v_and_b32_sdwa v67, v35, v38 dst_sel:DWORD dst_unused:UNUSED_PAD src0_sel:WORD_1 src1_sel:DWORD
	v_add3_u32 v35, v35, v67, s36
	s_waitcnt lgkmcnt(4)
	v_and_b32_sdwa v67, v76, v38 dst_sel:DWORD dst_unused:UNUSED_PAD src0_sel:WORD_1 src1_sel:DWORD
	v_and_b32_sdwa v68, v74, v38 dst_sel:DWORD dst_unused:UNUSED_PAD src0_sel:WORD_1 src1_sel:DWORD
	v_and_b32_sdwa v66, v75, v38 dst_sel:DWORD dst_unused:UNUSED_PAD src0_sel:WORD_1 src1_sel:DWORD
	v_add3_u32 v67, v76, v67, s36
	v_add3_u32 v68, v74, v68, s36
	v_add3_u32 v66, v75, v66, s36
	v_and_b32_e32 v67, 0xffff0000, v67
	v_and_b32_e32 v68, 0xffff0000, v68
	s_waitcnt lgkmcnt(0)
	v_and_b32_sdwa v69, v80, v38 dst_sel:DWORD dst_unused:UNUSED_PAD src0_sel:WORD_1 src1_sel:DWORD
	v_and_b32_sdwa v74, v78, v38 dst_sel:DWORD dst_unused:UNUSED_PAD src0_sel:WORD_1 src1_sel:DWORD
	v_or_b32_sdwa v67, v67, v66 dst_sel:DWORD dst_unused:UNUSED_PAD src0_sel:DWORD src1_sel:WORD_1
	v_or_b32_sdwa v66, v68, v35 dst_sel:DWORD dst_unused:UNUSED_PAD src0_sel:DWORD src1_sel:WORD_1
	v_and_b32_sdwa v35, v79, v38 dst_sel:DWORD dst_unused:UNUSED_PAD src0_sel:WORD_1 src1_sel:DWORD
	v_and_b32_sdwa v68, v77, v38 dst_sel:DWORD dst_unused:UNUSED_PAD src0_sel:WORD_1 src1_sel:DWORD
	v_add3_u32 v69, v80, v69, s36
	v_add3_u32 v74, v78, v74, s36
	v_add3_u32 v68, v77, v68, s36
	v_add3_u32 v35, v79, v35, s36
	v_and_b32_e32 v69, 0xffff0000, v69
	v_and_b32_e32 v74, 0xffff0000, v74
	v_or_b32_sdwa v69, v69, v35 dst_sel:DWORD dst_unused:UNUSED_PAD src0_sel:DWORD src1_sel:WORD_1
	v_or_b32_sdwa v68, v74, v68 dst_sel:DWORD dst_unused:UNUSED_PAD src0_sel:DWORD src1_sel:WORD_1
	global_store_dwordx4 v[72:73], v[66:69], off nt
	ds_read_b32 v35, v56
	ds_read_b32 v72, v56 offset:1028
	ds_read_b32 v73, v56 offset:2056
	ds_read_b32 v74, v56 offset:3084
	ds_read_b32 v75, v56 offset:4112
	ds_read_b32 v76, v56 offset:5140
	ds_read_b32 v77, v56 offset:6168
	ds_read_b32 v78, v56 offset:7196
	v_add_u32_e32 v66, s4, v55
	v_lshlrev_b32_e32 v67, 1, v66
	v_and_b32_e32 v67, 0xffffffe0, v67
	v_add3_u32 v67, s1, v57, v67
	v_cndmask_b32_e32 v66, v67, v66, vcc
	v_ashrrev_i32_e32 v69, 31, v66
	v_mad_u64_u32 v[66:67], s[2:3], v66, s30, 0
	v_mov_b32_e32 v68, v67
	v_mad_u64_u32 v[68:69], s[2:3], v69, s30, v[68:69]
	v_mov_b32_e32 v67, v68
	v_lshl_add_u64 v[70:71], v[66:67], 1, v[70:71]
	s_waitcnt lgkmcnt(7)
	v_and_b32_sdwa v67, v35, v38 dst_sel:DWORD dst_unused:UNUSED_PAD src0_sel:WORD_1 src1_sel:DWORD
	v_add3_u32 v35, v35, v67, s36
	s_waitcnt lgkmcnt(4)
	v_and_b32_sdwa v67, v74, v38 dst_sel:DWORD dst_unused:UNUSED_PAD src0_sel:WORD_1 src1_sel:DWORD
	v_and_b32_sdwa v68, v72, v38 dst_sel:DWORD dst_unused:UNUSED_PAD src0_sel:WORD_1 src1_sel:DWORD
	v_and_b32_sdwa v66, v73, v38 dst_sel:DWORD dst_unused:UNUSED_PAD src0_sel:WORD_1 src1_sel:DWORD
	v_add3_u32 v67, v74, v67, s36
	v_add3_u32 v68, v72, v68, s36
	v_add3_u32 v66, v73, v66, s36
	v_and_b32_e32 v67, 0xffff0000, v67
	v_and_b32_e32 v68, 0xffff0000, v68
	s_waitcnt lgkmcnt(0)
	v_and_b32_sdwa v69, v78, v38 dst_sel:DWORD dst_unused:UNUSED_PAD src0_sel:WORD_1 src1_sel:DWORD
	v_and_b32_sdwa v72, v76, v38 dst_sel:DWORD dst_unused:UNUSED_PAD src0_sel:WORD_1 src1_sel:DWORD
	v_or_b32_sdwa v67, v67, v66 dst_sel:DWORD dst_unused:UNUSED_PAD src0_sel:DWORD src1_sel:WORD_1
	v_or_b32_sdwa v66, v68, v35 dst_sel:DWORD dst_unused:UNUSED_PAD src0_sel:DWORD src1_sel:WORD_1
	v_and_b32_sdwa v35, v77, v38 dst_sel:DWORD dst_unused:UNUSED_PAD src0_sel:WORD_1 src1_sel:DWORD
	v_and_b32_sdwa v68, v75, v38 dst_sel:DWORD dst_unused:UNUSED_PAD src0_sel:WORD_1 src1_sel:DWORD
	v_add3_u32 v69, v78, v69, s36
	v_add3_u32 v72, v76, v72, s36
	v_add3_u32 v68, v75, v68, s36
	v_add3_u32 v35, v77, v35, s36
	v_and_b32_e32 v69, 0xffff0000, v69
	v_and_b32_e32 v72, 0xffff0000, v72
	v_or_b32_sdwa v69, v69, v35 dst_sel:DWORD dst_unused:UNUSED_PAD src0_sel:DWORD src1_sel:WORD_1
	v_or_b32_sdwa v68, v72, v68 dst_sel:DWORD dst_unused:UNUSED_PAD src0_sel:DWORD src1_sel:WORD_1
	s_add_i32 s34, s34, 1
	s_and_b64 vcc, exec, s[20:21]
	s_mov_b32 s28, s37
	s_mov_b32 s1, s39
	s_mov_b32 s19, s6
	s_mov_b32 s4, s24
	s_mov_b32 s18, s29
	s_mov_b32 s30, s38
	s_mov_b64 s[2:3], s[22:23]
	global_store_dwordx4 v[70:71], v[66:69], off nt
	s_barrier
	s_cbranch_vccnz .LBB0_3818
